# loop-edge rotation (guide 7.11): K-loop counter/pointer increments and exit test moved from behind the loop-back barrier into the last MFMA gaps (full units) / in front of the counted wait (half units
# speedup vs baseline: 1.0029x; 1.0029x over previous
.LBB0_252:
	ds_read_b128 v[40:43], v161
	ds_read_b128 v[44:47], v161 offset:1024
	ds_read_b128 v[56:59], v161 offset:2048
	ds_read_b128 v[60:63], v161 offset:3072
	ds_read_b128 v[148:151], v162
	ds_read_b128 v[152:155], v162 offset:1024
	ds_read_b128 v[164:167], v162 offset:2048
	ds_read_b128 v[168:171], v162 offset:3072
	s_add_u32 s25, s30, 0xfffa0080
	s_addc_u32 s34, s31, -1
	s_cmp_eq_u32 s23, 12
	s_cselect_b32 s35, s27, s34
	s_cselect_b32 s34, s26, s25
	s_cselect_b32 s40, s28, s5
	s_cselect_b32 s41, s29, s18
	s_add_u32 s38, s34, 0x80
	s_addc_u32 s39, s35, 0
	s_add_u32 s78, s30, 0xfffe0000
	v_mov_b32_e32 v146, v159
	s_addc_u32 s79, s31, -1
	ds_read_b128 v[172:175], v163
	ds_read_b128 v[176:179], v163 offset:1024
	ds_read_b128 v[180:183], v163 offset:2048
	ds_read_b128 v[184:187], v163 offset:3072
	ds_read_b128 v[188:191], v163 offset:4096
	ds_read_b128 v[192:195], v163 offset:5120
	ds_read_b128 v[196:199], v163 offset:6144
	ds_read_b128 v[200:203], v163 offset:7168
	s_add_i32 m0, s52, 0xc000
	s_nop 0
	global_load_lds_dwordx4 v146, s[78:79]
	s_mov_b64 s[78:79], s[30:31]
	s_add_i32 m0, s52, 0xe000
	s_nop 0
	global_load_lds_dwordx4 v159, s[78:79]
	s_waitcnt vmcnt(8)
	s_waitcnt lgkmcnt(0)
	s_barrier
	s_setprio 3
	v_mfma_f32_16x16x32_bf16 v[140:143], v[40:43], v[172:175], v[140:143]
	v_mfma_f32_16x16x32_bf16 v[132:135], v[56:59], v[172:175], v[132:135]
	v_mfma_f32_16x16x32_bf16 v[124:127], v[40:43], v[180:183], v[124:127]
	v_mfma_f32_16x16x32_bf16 v[116:119], v[56:59], v[180:183], v[116:119]
	v_mfma_f32_16x16x32_bf16 v[108:111], v[40:43], v[188:191], v[108:111]
	v_mfma_f32_16x16x32_bf16 v[100:103], v[56:59], v[188:191], v[100:103]
	v_mfma_f32_16x16x32_bf16 v[92:95], v[40:43], v[196:199], v[92:95]
	v_mfma_f32_16x16x32_bf16 v[84:87], v[56:59], v[196:199], v[84:87]
	v_mfma_f32_16x16x32_bf16 v[140:143], v[44:47], v[176:179], v[140:143]
	v_mfma_f32_16x16x32_bf16 v[132:135], v[60:63], v[176:179], v[132:135]
	v_mfma_f32_16x16x32_bf16 v[124:127], v[44:47], v[184:187], v[124:127]
	v_mfma_f32_16x16x32_bf16 v[116:119], v[60:63], v[184:187], v[116:119]
	v_mfma_f32_16x16x32_bf16 v[108:111], v[44:47], v[192:195], v[108:111]
	v_mfma_f32_16x16x32_bf16 v[100:103], v[60:63], v[192:195], v[100:103]
	v_mfma_f32_16x16x32_bf16 v[92:95], v[44:47], v[200:203], v[92:95]
	v_mfma_f32_16x16x32_bf16 v[84:87], v[60:63], v[200:203], v[84:87]
	v_mfma_f32_16x16x32_bf16 v[136:139], v[148:151], v[172:175], v[136:139]
	v_mfma_f32_16x16x32_bf16 v[128:131], v[164:167], v[172:175], v[128:131]
	v_mfma_f32_16x16x32_bf16 v[120:123], v[148:151], v[180:183], v[120:123]
	v_mfma_f32_16x16x32_bf16 v[112:115], v[164:167], v[180:183], v[112:115]
	v_mfma_f32_16x16x32_bf16 v[104:107], v[148:151], v[188:191], v[104:107]
	v_mfma_f32_16x16x32_bf16 v[96:99], v[164:167], v[188:191], v[96:99]
	v_mfma_f32_16x16x32_bf16 v[88:91], v[148:151], v[196:199], v[88:91]
	v_mfma_f32_16x16x32_bf16 v[80:83], v[164:167], v[196:199], v[80:83]
	v_mfma_f32_16x16x32_bf16 v[136:139], v[152:155], v[176:179], v[136:139]
	v_mfma_f32_16x16x32_bf16 v[128:131], v[168:171], v[176:179], v[128:131]
	v_mfma_f32_16x16x32_bf16 v[120:123], v[152:155], v[184:187], v[120:123]
	v_mfma_f32_16x16x32_bf16 v[112:115], v[168:171], v[184:187], v[112:115]
	v_mfma_f32_16x16x32_bf16 v[104:107], v[152:155], v[192:195], v[104:107]
	v_mfma_f32_16x16x32_bf16 v[96:99], v[168:171], v[192:195], v[96:99]
	v_mfma_f32_16x16x32_bf16 v[88:91], v[152:155], v[200:203], v[88:91]
	v_mfma_f32_16x16x32_bf16 v[80:83], v[168:171], v[200:203], v[80:83]
	s_setprio 0
	s_barrier
	v_mov_b32_e32 v146, v158
	s_mov_b64 s[78:79], s[40:41]
	s_add_i32 s25, s72, s51
	ds_read_b128 v[172:175], v163 offset:16384
	ds_read_b128 v[176:179], v163 offset:17408
	ds_read_b128 v[180:183], v163 offset:18432
	ds_read_b128 v[184:187], v163 offset:19456
	ds_read_b128 v[188:191], v163 offset:20480
	ds_read_b128 v[192:195], v163 offset:21504
	ds_read_b128 v[196:199], v163 offset:22528
	ds_read_b128 v[200:203], v163 offset:23552
	s_mov_b32 m0, s25
	s_nop 0
	global_load_lds_dwordx4 v146, s[78:79]
	s_add_u32 s78, s40, 0x20000
	s_addc_u32 s79, s41, 0
	s_add_i32 m0, s25, 0x2000
	s_nop 0
	global_load_lds_dwordx4 v158, s[78:79]
	s_add_u32 s78, s40, 0x40000
	s_addc_u32 s79, s41, 0
	s_add_i32 s25, s73, s51
	s_mov_b32 m0, s25
	s_nop 0
	global_load_lds_dwordx4 v158, s[78:79]
	s_add_u32 s78, s40, 0x60000
	s_addc_u32 s79, s41, 0
	s_add_i32 m0, s25, 0x2000
	s_nop 0
	global_load_lds_dwordx4 v158, s[78:79]
	s_mov_b64 s[78:79], s[34:35]
	s_mov_b32 m0, s52
	s_nop 0
	global_load_lds_dwordx4 v159, s[78:79]
	s_add_u32 s78, s34, 0x20000
	s_addc_u32 s79, s35, 0
	s_mov_b32 m0, s53
	s_nop 0
	global_load_lds_dwordx4 v159, s[78:79]
	s_waitcnt vmcnt(8)
	s_waitcnt lgkmcnt(0)
	s_barrier
	s_setprio 3
	v_mfma_f32_16x16x32_bf16 v[76:79], v[40:43], v[172:175], v[76:79]
	v_mfma_f32_16x16x32_bf16 v[68:71], v[56:59], v[172:175], v[68:71]
	v_mfma_f32_16x16x32_bf16 v[52:55], v[40:43], v[180:183], v[52:55]
	v_mfma_f32_16x16x32_bf16 v[36:39], v[56:59], v[180:183], v[36:39]
	v_mfma_f32_16x16x32_bf16 v[28:31], v[40:43], v[188:191], v[28:31]
	v_mfma_f32_16x16x32_bf16 v[20:23], v[56:59], v[188:191], v[20:23]
	v_mfma_f32_16x16x32_bf16 v[12:15], v[40:43], v[196:199], v[12:15]
	v_mfma_f32_16x16x32_bf16 v[4:7], v[56:59], v[196:199], v[4:7]
	v_mfma_f32_16x16x32_bf16 v[76:79], v[44:47], v[176:179], v[76:79]
	v_mfma_f32_16x16x32_bf16 v[68:71], v[60:63], v[176:179], v[68:71]
	v_mfma_f32_16x16x32_bf16 v[52:55], v[44:47], v[184:187], v[52:55]
	v_mfma_f32_16x16x32_bf16 v[36:39], v[60:63], v[184:187], v[36:39]
	v_mfma_f32_16x16x32_bf16 v[28:31], v[44:47], v[192:195], v[28:31]
	v_mfma_f32_16x16x32_bf16 v[20:23], v[60:63], v[192:195], v[20:23]
	v_mfma_f32_16x16x32_bf16 v[12:15], v[44:47], v[200:203], v[12:15]
	v_mfma_f32_16x16x32_bf16 v[4:7], v[60:63], v[200:203], v[4:7]
	v_mfma_f32_16x16x32_bf16 v[48:51], v[148:151], v[180:183], v[48:51]
	v_mfma_f32_16x16x32_bf16 v[32:35], v[164:167], v[180:183], v[32:35]
	v_mfma_f32_16x16x32_bf16 v[24:27], v[148:151], v[188:191], v[24:27]
	v_mfma_f32_16x16x32_bf16 v[16:19], v[164:167], v[188:191], v[16:19]
	v_mfma_f32_16x16x32_bf16 v[8:11], v[148:151], v[196:199], v[8:11]
	v_mfma_f32_16x16x32_bf16 v[0:3], v[164:167], v[196:199], v[0:3]
	v_mfma_f32_16x16x32_bf16 v[40:43], v[148:151], v[172:175], v[72:75]
	v_mfma_f32_16x16x32_bf16 v[44:47], v[164:167], v[172:175], v[64:67]
	v_mfma_f32_16x16x32_bf16 v[48:51], v[152:155], v[184:187], v[48:51]
	v_mfma_f32_16x16x32_bf16 v[32:35], v[168:171], v[184:187], v[32:35]
	v_mfma_f32_16x16x32_bf16 v[24:27], v[152:155], v[192:195], v[24:27]
	v_mfma_f32_16x16x32_bf16 v[16:19], v[168:171], v[192:195], v[16:19]
	v_mfma_f32_16x16x32_bf16 v[8:11], v[152:155], v[200:203], v[8:11]
	v_mfma_f32_16x16x32_bf16 v[0:3], v[168:171], v[200:203], v[0:3]
	v_mfma_f32_16x16x32_bf16 v[40:43], v[152:155], v[176:179], v[40:43]
	v_mfma_f32_16x16x32_bf16 v[44:47], v[168:171], v[176:179], v[44:47]
	s_setprio 0
	s_barrier
	s_add_i32 s25, 0, 0x18000
	s_add_i32 s37, 0, 0x1c000
	v_add_u32_e32 v72, s25, v160
	v_add_u32_e32 v146, s37, v160
	ds_read_b128 v[56:59], v72
	ds_read_b128 v[60:63], v72 offset:1024
	ds_read_b128 v[64:67], v72 offset:2048
	ds_read_b128 v[72:75], v72 offset:3072
	ds_read_b128 v[148:151], v146
	ds_read_b128 v[152:155], v146 offset:1024
	ds_read_b128 v[164:167], v146 offset:2048
	ds_read_b128 v[168:171], v146 offset:3072
	s_add_u32 s78, s34, 0x40000
	v_mov_b32_e32 v146, v159
	s_addc_u32 s79, s35, 0
	s_mov_b32 m0, s60
	ds_read_b128 v[172:175], v163 offset:32768
	ds_read_b128 v[176:179], v163 offset:33792
	ds_read_b128 v[180:183], v163 offset:34816
	ds_read_b128 v[184:187], v163 offset:35840
	ds_read_b128 v[188:191], v163 offset:36864
	ds_read_b128 v[192:195], v163 offset:37888
	ds_read_b128 v[196:199], v163 offset:38912
	ds_read_b128 v[200:203], v163 offset:39936
	s_nop 0
	global_load_lds_dwordx4 v146, s[78:79]
	s_add_u32 s78, s34, 0x60000
	s_addc_u32 s79, s35, 0
	s_mov_b32 m0, s61
	s_nop 0
	global_load_lds_dwordx4 v159, s[78:79]
	s_waitcnt vmcnt(8)
	s_waitcnt lgkmcnt(0)
	s_barrier
	s_setprio 3
	v_mfma_f32_16x16x32_bf16 v[140:143], v[56:59], v[172:175], v[140:143]
	v_mfma_f32_16x16x32_bf16 v[132:135], v[64:67], v[172:175], v[132:135]
	v_mfma_f32_16x16x32_bf16 v[124:127], v[56:59], v[180:183], v[124:127]
	v_mfma_f32_16x16x32_bf16 v[116:119], v[64:67], v[180:183], v[116:119]
	v_mfma_f32_16x16x32_bf16 v[108:111], v[56:59], v[188:191], v[108:111]
	v_mfma_f32_16x16x32_bf16 v[100:103], v[64:67], v[188:191], v[100:103]
	v_mfma_f32_16x16x32_bf16 v[92:95], v[56:59], v[196:199], v[92:95]
	v_mfma_f32_16x16x32_bf16 v[84:87], v[64:67], v[196:199], v[84:87]
	v_mfma_f32_16x16x32_bf16 v[140:143], v[60:63], v[176:179], v[140:143]
	v_mfma_f32_16x16x32_bf16 v[132:135], v[72:75], v[176:179], v[132:135]
	v_mfma_f32_16x16x32_bf16 v[124:127], v[60:63], v[184:187], v[124:127]
	v_mfma_f32_16x16x32_bf16 v[116:119], v[72:75], v[184:187], v[116:119]
	v_mfma_f32_16x16x32_bf16 v[108:111], v[60:63], v[192:195], v[108:111]
	v_mfma_f32_16x16x32_bf16 v[100:103], v[72:75], v[192:195], v[100:103]
	v_mfma_f32_16x16x32_bf16 v[92:95], v[60:63], v[200:203], v[92:95]
	v_mfma_f32_16x16x32_bf16 v[84:87], v[72:75], v[200:203], v[84:87]
	v_mfma_f32_16x16x32_bf16 v[136:139], v[148:151], v[172:175], v[136:139]
	v_mfma_f32_16x16x32_bf16 v[128:131], v[164:167], v[172:175], v[128:131]
	v_mfma_f32_16x16x32_bf16 v[120:123], v[148:151], v[180:183], v[120:123]
	v_mfma_f32_16x16x32_bf16 v[112:115], v[164:167], v[180:183], v[112:115]
	v_mfma_f32_16x16x32_bf16 v[104:107], v[148:151], v[188:191], v[104:107]
	v_mfma_f32_16x16x32_bf16 v[96:99], v[164:167], v[188:191], v[96:99]
	v_mfma_f32_16x16x32_bf16 v[88:91], v[148:151], v[196:199], v[88:91]
	v_mfma_f32_16x16x32_bf16 v[80:83], v[164:167], v[196:199], v[80:83]
	v_mfma_f32_16x16x32_bf16 v[136:139], v[152:155], v[176:179], v[136:139]
	v_mfma_f32_16x16x32_bf16 v[128:131], v[168:171], v[176:179], v[128:131]
	v_mfma_f32_16x16x32_bf16 v[120:123], v[152:155], v[184:187], v[120:123]
	v_mfma_f32_16x16x32_bf16 v[112:115], v[168:171], v[184:187], v[112:115]
	v_mfma_f32_16x16x32_bf16 v[104:107], v[152:155], v[192:195], v[104:107]
	v_mfma_f32_16x16x32_bf16 v[96:99], v[168:171], v[192:195], v[96:99]
	v_mfma_f32_16x16x32_bf16 v[88:91], v[152:155], v[200:203], v[88:91]
	v_mfma_f32_16x16x32_bf16 v[80:83], v[168:171], v[200:203], v[80:83]
	s_setprio 0
	s_barrier
	s_add_u32 s78, s40, 0x80
	s_addc_u32 s79, s41, 0
	v_mov_b32_e32 v146, v158
	s_add_i32 s25, s25, s51
	ds_read_b128 v[172:175], v163 offset:49152
	ds_read_b128 v[176:179], v163 offset:50176
	ds_read_b128 v[180:183], v163 offset:51200
	ds_read_b128 v[184:187], v163 offset:52224
	ds_read_b128 v[188:191], v163 offset:53248
	ds_read_b128 v[192:195], v163 offset:54272
	ds_read_b128 v[196:199], v163 offset:55296
	ds_read_b128 v[200:203], v163 offset:56320
	s_mov_b32 m0, s25
	s_nop 0
	global_load_lds_dwordx4 v146, s[78:79]
	s_add_u32 s78, s40, 0x20080
	s_addc_u32 s79, s41, 0
	s_add_i32 m0, s25, 0x2000
	s_nop 0
	global_load_lds_dwordx4 v158, s[78:79]
	s_add_u32 s78, s40, 0x40080
	s_addc_u32 s79, s41, 0
	s_add_i32 s25, s37, s51
	s_mov_b32 m0, s25
	s_add_u32 s40, s40, 0x60080
	global_load_lds_dwordx4 v158, s[78:79]
	s_addc_u32 s41, s41, 0
	s_add_i32 m0, s25, 0x2000
	s_add_u32 s34, s34, 0x20080
	global_load_lds_dwordx4 v158, s[40:41]
	s_mov_b32 m0, s69
	s_addc_u32 s35, s35, 0
	global_load_lds_dwordx4 v159, s[38:39]
	s_mov_b32 m0, s70
	s_nop 0
	global_load_lds_dwordx4 v159, s[34:35]
	s_waitcnt vmcnt(8)
	s_waitcnt lgkmcnt(0)
	s_barrier
	s_setprio 3
	v_mfma_f32_16x16x32_bf16 v[76:79], v[56:59], v[172:175], v[76:79]
	v_mfma_f32_16x16x32_bf16 v[68:71], v[64:67], v[172:175], v[68:71]
	v_mfma_f32_16x16x32_bf16 v[52:55], v[56:59], v[180:183], v[52:55]
	v_mfma_f32_16x16x32_bf16 v[36:39], v[64:67], v[180:183], v[36:39]
	v_mfma_f32_16x16x32_bf16 v[28:31], v[56:59], v[188:191], v[28:31]
	v_mfma_f32_16x16x32_bf16 v[20:23], v[64:67], v[188:191], v[20:23]
	v_mfma_f32_16x16x32_bf16 v[12:15], v[56:59], v[196:199], v[12:15]
	v_mfma_f32_16x16x32_bf16 v[4:7], v[64:67], v[196:199], v[4:7]
	v_mfma_f32_16x16x32_bf16 v[76:79], v[60:63], v[176:179], v[76:79]
	v_mfma_f32_16x16x32_bf16 v[68:71], v[72:75], v[176:179], v[68:71]
	v_mfma_f32_16x16x32_bf16 v[52:55], v[60:63], v[184:187], v[52:55]
	v_mfma_f32_16x16x32_bf16 v[36:39], v[72:75], v[184:187], v[36:39]
	v_mfma_f32_16x16x32_bf16 v[28:31], v[60:63], v[192:195], v[28:31]
	v_mfma_f32_16x16x32_bf16 v[20:23], v[72:75], v[192:195], v[20:23]
	v_mfma_f32_16x16x32_bf16 v[12:15], v[60:63], v[200:203], v[12:15]
	v_mfma_f32_16x16x32_bf16 v[4:7], v[72:75], v[200:203], v[4:7]
	v_mfma_f32_16x16x32_bf16 v[40:43], v[148:151], v[172:175], v[40:43]
	v_mfma_f32_16x16x32_bf16 v[72:75], v[152:155], v[176:179], v[40:43]
	v_mfma_f32_16x16x32_bf16 v[40:43], v[164:167], v[172:175], v[44:47]
	v_mfma_f32_16x16x32_bf16 v[64:67], v[168:171], v[176:179], v[40:43]
	v_mfma_f32_16x16x32_bf16 v[40:43], v[148:151], v[180:183], v[48:51]
	v_mfma_f32_16x16x32_bf16 v[32:35], v[164:167], v[180:183], v[32:35]
	v_mfma_f32_16x16x32_bf16 v[24:27], v[148:151], v[188:191], v[24:27]
	v_mfma_f32_16x16x32_bf16 v[16:19], v[164:167], v[188:191], v[16:19]
	v_mfma_f32_16x16x32_bf16 v[8:11], v[148:151], v[196:199], v[8:11]
	s_add_i32 s23, s23, 2
	v_mfma_f32_16x16x32_bf16 v[0:3], v[164:167], v[196:199], v[0:3]
	s_add_u32 s5, s5, 0x100
	v_mfma_f32_16x16x32_bf16 v[48:51], v[152:155], v[184:187], v[40:43]
	s_addc_u32 s18, s18, 0
	v_mfma_f32_16x16x32_bf16 v[32:35], v[168:171], v[184:187], v[32:35]
	s_add_u32 s30, s30, 0x100
	v_mfma_f32_16x16x32_bf16 v[24:27], v[152:155], v[192:195], v[24:27]
	s_addc_u32 s31, s31, 0
	v_mfma_f32_16x16x32_bf16 v[16:19], v[168:171], v[192:195], v[16:19]
	s_cmp_gt_u32 s23, 13
	v_mfma_f32_16x16x32_bf16 v[8:11], v[152:155], v[200:203], v[8:11]
	v_mfma_f32_16x16x32_bf16 v[0:3], v[168:171], v[200:203], v[0:3]
	s_setprio 0
	s_barrier
	s_cbranch_scc0 .LBB0_252
	s_and_b64 vcc, exec, s[20:21]
	s_cbranch_vccz .LBB0_255
	s_barrier

.LBB0_333:
	ds_read_b128 v[52:55], v38
	ds_read_b128 v[56:59], v38 offset:1024
	ds_read_b128 v[80:83], v38 offset:2048
	ds_read_b128 v[84:87], v38 offset:3072
	ds_read_b128 v[88:91], v39
	ds_read_b128 v[92:95], v39 offset:1024
	ds_read_b128 v[96:99], v39 offset:2048
	ds_read_b128 v[100:103], v39 offset:3072
	s_cmp_eq_u32 s34, 12
	s_cselect_b32 s14, s4, s30
	s_cselect_b32 s15, s5, s31
	s_cselect_b32 s18, s12, s28
	s_cselect_b32 s19, s13, s29
	s_add_u32 s16, s14, 0x80
	s_addc_u32 s17, s15, 0
	ds_read_b128 v[104:107], v40
	ds_read_b128 v[108:111], v40 offset:1024
	ds_read_b128 v[112:115], v40 offset:2048
	ds_read_b128 v[116:119], v40 offset:3072
	ds_read_b128 v[120:123], v40 offset:4096
	ds_read_b128 v[124:127], v40 offset:5120
	ds_read_b128 v[128:131], v40 offset:6144
	ds_read_b128 v[132:135], v40 offset:7168
	s_waitcnt vmcnt(6)
	s_waitcnt lgkmcnt(0)
	s_barrier
	s_setprio 3
	v_mfma_f32_16x16x32_bf16 v[76:79], v[52:55], v[104:107], v[76:79]
	v_mfma_f32_16x16x32_bf16 v[68:71], v[80:83], v[104:107], v[68:71]
	v_mfma_f32_16x16x32_bf16 v[60:63], v[52:55], v[112:115], v[60:63]
	v_mfma_f32_16x16x32_bf16 v[44:47], v[80:83], v[112:115], v[44:47]
	v_mfma_f32_16x16x32_bf16 v[28:31], v[52:55], v[120:123], v[28:31]
	v_mfma_f32_16x16x32_bf16 v[20:23], v[80:83], v[120:123], v[20:23]
	v_mfma_f32_16x16x32_bf16 v[12:15], v[52:55], v[128:131], v[12:15]
	v_mfma_f32_16x16x32_bf16 v[4:7], v[80:83], v[128:131], v[4:7]
	v_mfma_f32_16x16x32_bf16 v[76:79], v[56:59], v[108:111], v[76:79]
	v_mfma_f32_16x16x32_bf16 v[68:71], v[84:87], v[108:111], v[68:71]
	v_mfma_f32_16x16x32_bf16 v[60:63], v[56:59], v[116:119], v[60:63]
	v_mfma_f32_16x16x32_bf16 v[44:47], v[84:87], v[116:119], v[44:47]
	v_mfma_f32_16x16x32_bf16 v[28:31], v[56:59], v[124:127], v[28:31]
	v_mfma_f32_16x16x32_bf16 v[20:23], v[84:87], v[124:127], v[20:23]
	v_mfma_f32_16x16x32_bf16 v[12:15], v[56:59], v[132:135], v[12:15]
	v_mfma_f32_16x16x32_bf16 v[4:7], v[84:87], v[132:135], v[4:7]
	v_mfma_f32_16x16x32_bf16 v[48:51], v[88:91], v[112:115], v[48:51]
	v_mfma_f32_16x16x32_bf16 v[32:35], v[96:99], v[112:115], v[32:35]
	v_mfma_f32_16x16x32_bf16 v[24:27], v[88:91], v[120:123], v[24:27]
	v_mfma_f32_16x16x32_bf16 v[16:19], v[96:99], v[120:123], v[16:19]
	v_mfma_f32_16x16x32_bf16 v[8:11], v[88:91], v[128:131], v[8:11]
	v_mfma_f32_16x16x32_bf16 v[0:3], v[96:99], v[128:131], v[0:3]
	v_mfma_f32_16x16x32_bf16 v[52:55], v[88:91], v[104:107], v[72:75]
	v_mfma_f32_16x16x32_bf16 v[56:59], v[96:99], v[104:107], v[64:67]
	v_mfma_f32_16x16x32_bf16 v[48:51], v[92:95], v[116:119], v[48:51]
	v_mfma_f32_16x16x32_bf16 v[32:35], v[100:103], v[116:119], v[32:35]
	v_mfma_f32_16x16x32_bf16 v[24:27], v[92:95], v[124:127], v[24:27]
	v_mfma_f32_16x16x32_bf16 v[16:19], v[100:103], v[124:127], v[16:19]
	v_mfma_f32_16x16x32_bf16 v[8:11], v[92:95], v[132:135], v[8:11]
	v_mfma_f32_16x16x32_bf16 v[0:3], v[100:103], v[132:135], v[0:3]
	v_mfma_f32_16x16x32_bf16 v[52:55], v[92:95], v[108:111], v[52:55]
	v_mfma_f32_16x16x32_bf16 v[56:59], v[100:103], v[108:111], v[56:59]
	s_setprio 0
	s_barrier
	s_mov_b64 s[50:51], s[18:19]
	s_mov_b32 m0, s35
	s_nop 0
	global_load_lds_dwordx4 v36, s[50:51]
	s_add_u32 s50, s18, 0x20000
	s_addc_u32 s51, s19, 0
	s_mov_b32 m0, s36
	s_nop 0
	global_load_lds_dwordx4 v36, s[50:51]
	s_add_u32 s50, s18, 0x40000
	s_addc_u32 s51, s19, 0
	s_mov_b32 m0, s37
	s_nop 0
	global_load_lds_dwordx4 v36, s[50:51]
	s_add_u32 s50, s18, 0x60000
	s_addc_u32 s51, s19, 0
	s_mov_b32 m0, s38
	s_nop 0
	global_load_lds_dwordx4 v36, s[50:51]
	s_mov_b64 s[50:51], s[14:15]
	s_mov_b32 m0, s23
	s_nop 0
	global_load_lds_dwordx4 v37, s[50:51]
	s_add_u32 s50, s14, 0x20000
	s_addc_u32 s51, s15, 0
	s_mov_b32 m0, s24
	s_nop 0
	global_load_lds_dwordx4 v37, s[50:51]
	s_waitcnt vmcnt(6)
	s_waitcnt lgkmcnt(0)
	s_barrier
	s_barrier
	ds_read_b128 v[64:67], v41
	ds_read_b128 v[72:75], v41 offset:1024
	ds_read_b128 v[80:83], v41 offset:2048
	ds_read_b128 v[84:87], v41 offset:3072
	ds_read_b128 v[88:91], v42
	ds_read_b128 v[92:95], v42 offset:1024
	ds_read_b128 v[96:99], v42 offset:2048
	ds_read_b128 v[100:103], v42 offset:3072
	ds_read_b128 v[104:107], v40 offset:32768
	ds_read_b128 v[108:111], v40 offset:33792
	ds_read_b128 v[112:115], v40 offset:34816
	ds_read_b128 v[116:119], v40 offset:35840
	ds_read_b128 v[120:123], v40 offset:36864
	ds_read_b128 v[124:127], v40 offset:37888
	ds_read_b128 v[128:131], v40 offset:38912
	ds_read_b128 v[132:135], v40 offset:39936
	s_waitcnt vmcnt(6)
	s_waitcnt lgkmcnt(0)
	s_barrier
	s_setprio 3
	v_mfma_f32_16x16x32_bf16 v[76:79], v[64:67], v[104:107], v[76:79]
	v_mfma_f32_16x16x32_bf16 v[68:71], v[80:83], v[104:107], v[68:71]
	v_mfma_f32_16x16x32_bf16 v[60:63], v[64:67], v[112:115], v[60:63]
	v_mfma_f32_16x16x32_bf16 v[44:47], v[80:83], v[112:115], v[44:47]
	v_mfma_f32_16x16x32_bf16 v[28:31], v[64:67], v[120:123], v[28:31]
	v_mfma_f32_16x16x32_bf16 v[20:23], v[80:83], v[120:123], v[20:23]
	v_mfma_f32_16x16x32_bf16 v[12:15], v[64:67], v[128:131], v[12:15]
	v_mfma_f32_16x16x32_bf16 v[4:7], v[80:83], v[128:131], v[4:7]
	v_mfma_f32_16x16x32_bf16 v[76:79], v[72:75], v[108:111], v[76:79]
	v_mfma_f32_16x16x32_bf16 v[68:71], v[84:87], v[108:111], v[68:71]
	v_mfma_f32_16x16x32_bf16 v[60:63], v[72:75], v[116:119], v[60:63]
	v_mfma_f32_16x16x32_bf16 v[44:47], v[84:87], v[116:119], v[44:47]
	v_mfma_f32_16x16x32_bf16 v[28:31], v[72:75], v[124:127], v[28:31]
	v_mfma_f32_16x16x32_bf16 v[20:23], v[84:87], v[124:127], v[20:23]
	v_mfma_f32_16x16x32_bf16 v[12:15], v[72:75], v[132:135], v[12:15]
	v_mfma_f32_16x16x32_bf16 v[4:7], v[84:87], v[132:135], v[4:7]
	v_mfma_f32_16x16x32_bf16 v[52:55], v[88:91], v[104:107], v[52:55]
	s_add_u32 s50, s18, 0x80
	s_addc_u32 s51, s19, 0
	v_mfma_f32_16x16x32_bf16 v[72:75], v[92:95], v[108:111], v[52:55]
	v_mfma_f32_16x16x32_bf16 v[52:55], v[96:99], v[104:107], v[56:59]
	v_mfma_f32_16x16x32_bf16 v[48:51], v[88:91], v[112:115], v[48:51]
	v_mfma_f32_16x16x32_bf16 v[32:35], v[96:99], v[112:115], v[32:35]
	v_mfma_f32_16x16x32_bf16 v[24:27], v[88:91], v[120:123], v[24:27]
	v_mfma_f32_16x16x32_bf16 v[16:19], v[96:99], v[120:123], v[16:19]
	v_mfma_f32_16x16x32_bf16 v[8:11], v[88:91], v[128:131], v[8:11]
	v_mfma_f32_16x16x32_bf16 v[0:3], v[96:99], v[128:131], v[0:3]
	v_mfma_f32_16x16x32_bf16 v[64:67], v[100:103], v[108:111], v[52:55]
	v_mfma_f32_16x16x32_bf16 v[48:51], v[92:95], v[116:119], v[48:51]
	v_mfma_f32_16x16x32_bf16 v[32:35], v[100:103], v[116:119], v[32:35]
	v_mfma_f32_16x16x32_bf16 v[24:27], v[92:95], v[124:127], v[24:27]
	v_mfma_f32_16x16x32_bf16 v[16:19], v[100:103], v[124:127], v[16:19]
	v_mfma_f32_16x16x32_bf16 v[8:11], v[92:95], v[132:135], v[8:11]
	v_mfma_f32_16x16x32_bf16 v[0:3], v[100:103], v[132:135], v[0:3]
	s_setprio 0
	s_barrier
	s_mov_b32 m0, s39
	s_nop 0
	global_load_lds_dwordx4 v36, s[50:51]
	s_add_u32 s50, s18, 0x20080
	s_addc_u32 s51, s19, 0
	s_mov_b32 m0, s40
	s_nop 0
	global_load_lds_dwordx4 v36, s[50:51]
	s_add_u32 s50, s18, 0x40080
	s_addc_u32 s51, s19, 0
	s_mov_b32 m0, s41
	s_add_u32 s18, s18, 0x60080
	global_load_lds_dwordx4 v36, s[50:51]
	s_addc_u32 s19, s19, 0
	s_mov_b32 m0, s49
	s_add_u32 s14, s14, 0x20080
	global_load_lds_dwordx4 v36, s[18:19]
	s_mov_b32 m0, s26
	s_addc_u32 s15, s15, 0
	global_load_lds_dwordx4 v37, s[16:17]
	s_mov_b32 m0, s27
	s_nop 0
	global_load_lds_dwordx4 v37, s[14:15]
	s_add_i32 s34, s34, 2
	s_add_u32 s28, s28, 0x100
	s_addc_u32 s29, s29, 0
	s_add_u32 s30, s30, 0x100
	s_addc_u32 s31, s31, 0
	s_cmp_gt_u32 s34, 13
	s_waitcnt vmcnt(6)
	s_waitcnt lgkmcnt(0)
	s_barrier
	s_barrier
	s_cbranch_scc0 .LBB0_333
	s_cmpk_lt_u32 s1, 0x100
	s_cbranch_scc0 .LBB0_336
	s_barrier

.LBB0_725:
	ds_read_b128 v[130:133], v177
	ds_read_b128 v[134:137], v177 offset:1024
	ds_read_b128 v[138:141], v177 offset:2048
	ds_read_b128 v[142:145], v177 offset:3072
	ds_read_b128 v[146:149], v178
	ds_read_b128 v[150:153], v178 offset:1024
	ds_read_b128 v[154:157], v178 offset:2048
	ds_read_b128 v[158:161], v178 offset:3072
	s_add_u32 s26, s24, 0xfffa0080
	s_addc_u32 s27, s25, -1
	s_cmp_eq_u32 s60, 12
	s_cselect_b32 s26, s18, s26
	s_cselect_b32 s27, s19, s27
	s_cselect_b32 s30, s20, s15
	s_cselect_b32 s31, s21, s17
	s_add_u32 s28, s26, 0x80
	s_addc_u32 s29, s27, 0
	s_add_u32 s64, s24, 0xfffe0000
	v_mov_b32_e32 v200, v175
	s_addc_u32 s65, s25, -1
	ds_read_b128 v[162:165], v179
	ds_read_b128 v[166:169], v179 offset:1024
	ds_read_b128 v[170:173], v179 offset:2048
	ds_read_b128 v[180:183], v179 offset:3072
	ds_read_b128 v[184:187], v179 offset:4096
	ds_read_b128 v[188:191], v179 offset:5120
	ds_read_b128 v[192:195], v179 offset:6144
	ds_read_b128 v[196:199], v179 offset:7168
	s_add_i32 m0, s23, 0xc000
	s_nop 0
	global_load_lds_dwordx4 v200, s[64:65]
	s_mov_b64 s[64:65], s[24:25]
	s_add_i32 m0, s23, 0xe000
	s_nop 0
	global_load_lds_dwordx4 v175, s[64:65]
	s_waitcnt vmcnt(8)
	s_waitcnt lgkmcnt(0)
	s_barrier
	s_setprio 3
	v_mfma_f32_16x16x32_bf16 v[124:127], v[130:133], v[162:165], v[124:127]
	v_mfma_f32_16x16x32_bf16 v[120:123], v[138:141], v[162:165], v[120:123]
	v_mfma_f32_16x16x32_bf16 v[108:111], v[130:133], v[170:173], v[108:111]
	v_mfma_f32_16x16x32_bf16 v[104:107], v[138:141], v[170:173], v[104:107]
	v_mfma_f32_16x16x32_bf16 v[92:95], v[130:133], v[184:187], v[92:95]
	v_mfma_f32_16x16x32_bf16 v[88:91], v[138:141], v[184:187], v[88:91]
	v_mfma_f32_16x16x32_bf16 v[76:79], v[130:133], v[192:195], v[76:79]
	v_mfma_f32_16x16x32_bf16 v[72:75], v[138:141], v[192:195], v[72:75]
	v_mfma_f32_16x16x32_bf16 v[124:127], v[134:137], v[166:169], v[124:127]
	v_mfma_f32_16x16x32_bf16 v[120:123], v[142:145], v[166:169], v[120:123]
	v_mfma_f32_16x16x32_bf16 v[108:111], v[134:137], v[180:183], v[108:111]
	v_mfma_f32_16x16x32_bf16 v[104:107], v[142:145], v[180:183], v[104:107]
	v_mfma_f32_16x16x32_bf16 v[92:95], v[134:137], v[188:191], v[92:95]
	v_mfma_f32_16x16x32_bf16 v[88:91], v[142:145], v[188:191], v[88:91]
	v_mfma_f32_16x16x32_bf16 v[76:79], v[134:137], v[196:199], v[76:79]
	v_mfma_f32_16x16x32_bf16 v[72:75], v[142:145], v[196:199], v[72:75]
	v_mfma_f32_16x16x32_bf16 v[116:119], v[146:149], v[162:165], v[116:119]
	v_mfma_f32_16x16x32_bf16 v[112:115], v[154:157], v[162:165], v[112:115]
	v_mfma_f32_16x16x32_bf16 v[100:103], v[146:149], v[170:173], v[100:103]
	v_mfma_f32_16x16x32_bf16 v[96:99], v[154:157], v[170:173], v[96:99]
	v_mfma_f32_16x16x32_bf16 v[84:87], v[146:149], v[184:187], v[84:87]
	v_mfma_f32_16x16x32_bf16 v[80:83], v[154:157], v[184:187], v[80:83]
	v_mfma_f32_16x16x32_bf16 v[68:71], v[146:149], v[192:195], v[68:71]
	v_mfma_f32_16x16x32_bf16 v[64:67], v[154:157], v[192:195], v[64:67]
	v_mfma_f32_16x16x32_bf16 v[116:119], v[150:153], v[166:169], v[116:119]
	v_mfma_f32_16x16x32_bf16 v[112:115], v[158:161], v[166:169], v[112:115]
	v_mfma_f32_16x16x32_bf16 v[100:103], v[150:153], v[180:183], v[100:103]
	v_mfma_f32_16x16x32_bf16 v[96:99], v[158:161], v[180:183], v[96:99]
	v_mfma_f32_16x16x32_bf16 v[84:87], v[150:153], v[188:191], v[84:87]
	v_mfma_f32_16x16x32_bf16 v[80:83], v[158:161], v[188:191], v[80:83]
	v_mfma_f32_16x16x32_bf16 v[68:71], v[150:153], v[196:199], v[68:71]
	v_mfma_f32_16x16x32_bf16 v[64:67], v[158:161], v[196:199], v[64:67]
	s_setprio 0
	s_barrier
	v_mov_b32_e32 v200, v174
	s_mov_b64 s[64:65], s[30:31]
	s_add_i32 s61, s51, s36
	ds_read_b128 v[162:165], v179 offset:16384
	ds_read_b128 v[166:169], v179 offset:17408
	ds_read_b128 v[170:173], v179 offset:18432
	ds_read_b128 v[180:183], v179 offset:19456
	ds_read_b128 v[184:187], v179 offset:20480
	ds_read_b128 v[188:191], v179 offset:21504
	ds_read_b128 v[192:195], v179 offset:22528
	ds_read_b128 v[196:199], v179 offset:23552
	s_mov_b32 m0, s61
	s_nop 0
	global_load_lds_dwordx4 v200, s[64:65]
	s_add_u32 s64, s30, 0x20000
	s_addc_u32 s65, s31, 0
	s_add_i32 m0, s61, 0x2000
	s_nop 0
	global_load_lds_dwordx4 v174, s[64:65]
	s_add_u32 s64, s30, 0x40000
	s_addc_u32 s65, s31, 0
	s_add_i32 s61, s52, s36
	s_mov_b32 m0, s61
	s_nop 0
	global_load_lds_dwordx4 v174, s[64:65]
	s_add_u32 s64, s30, 0x60000
	s_addc_u32 s65, s31, 0
	s_add_i32 m0, s61, 0x2000
	s_nop 0
	global_load_lds_dwordx4 v174, s[64:65]
	s_mov_b64 s[64:65], s[26:27]
	s_mov_b32 m0, s23
	s_nop 0
	global_load_lds_dwordx4 v175, s[64:65]
	s_add_u32 s64, s26, 0x20000
	s_addc_u32 s65, s27, 0
	s_mov_b32 m0, s38
	s_nop 0
	global_load_lds_dwordx4 v175, s[64:65]
	s_waitcnt vmcnt(8)
	s_waitcnt lgkmcnt(0)
	s_barrier
	s_setprio 3
	v_mfma_f32_16x16x32_bf16 v[60:63], v[130:133], v[162:165], v[60:63]
	v_mfma_f32_16x16x32_bf16 v[56:59], v[138:141], v[162:165], v[56:59]
	v_mfma_f32_16x16x32_bf16 v[44:47], v[130:133], v[170:173], v[44:47]
	v_mfma_f32_16x16x32_bf16 v[40:43], v[138:141], v[170:173], v[40:43]
	v_mfma_f32_16x16x32_bf16 v[28:31], v[130:133], v[184:187], v[28:31]
	v_mfma_f32_16x16x32_bf16 v[24:27], v[138:141], v[184:187], v[24:27]
	v_mfma_f32_16x16x32_bf16 v[12:15], v[130:133], v[192:195], v[12:15]
	v_mfma_f32_16x16x32_bf16 v[8:11], v[138:141], v[192:195], v[8:11]
	v_mfma_f32_16x16x32_bf16 v[60:63], v[134:137], v[166:169], v[60:63]
	v_mfma_f32_16x16x32_bf16 v[56:59], v[142:145], v[166:169], v[56:59]
	v_mfma_f32_16x16x32_bf16 v[44:47], v[134:137], v[180:183], v[44:47]
	v_mfma_f32_16x16x32_bf16 v[40:43], v[142:145], v[180:183], v[40:43]
	v_mfma_f32_16x16x32_bf16 v[28:31], v[134:137], v[188:191], v[28:31]
	v_mfma_f32_16x16x32_bf16 v[24:27], v[142:145], v[188:191], v[24:27]
	v_mfma_f32_16x16x32_bf16 v[12:15], v[134:137], v[196:199], v[12:15]
	v_mfma_f32_16x16x32_bf16 v[8:11], v[142:145], v[196:199], v[8:11]
	v_mfma_f32_16x16x32_bf16 v[52:55], v[146:149], v[162:165], v[52:55]
	v_mfma_f32_16x16x32_bf16 v[48:51], v[154:157], v[162:165], v[48:51]
	v_mfma_f32_16x16x32_bf16 v[36:39], v[146:149], v[170:173], v[36:39]
	v_mfma_f32_16x16x32_bf16 v[32:35], v[154:157], v[170:173], v[32:35]
	v_mfma_f32_16x16x32_bf16 v[20:23], v[146:149], v[184:187], v[20:23]
	v_mfma_f32_16x16x32_bf16 v[16:19], v[154:157], v[184:187], v[16:19]
	v_mfma_f32_16x16x32_bf16 v[4:7], v[146:149], v[192:195], v[4:7]
	v_mfma_f32_16x16x32_bf16 v[0:3], v[154:157], v[192:195], v[0:3]
	v_mfma_f32_16x16x32_bf16 v[52:55], v[150:153], v[166:169], v[52:55]
	v_mfma_f32_16x16x32_bf16 v[48:51], v[158:161], v[166:169], v[48:51]
	v_mfma_f32_16x16x32_bf16 v[36:39], v[150:153], v[180:183], v[36:39]
	v_mfma_f32_16x16x32_bf16 v[32:35], v[158:161], v[180:183], v[32:35]
	v_mfma_f32_16x16x32_bf16 v[20:23], v[150:153], v[188:191], v[20:23]
	v_mfma_f32_16x16x32_bf16 v[16:19], v[158:161], v[188:191], v[16:19]
	v_mfma_f32_16x16x32_bf16 v[4:7], v[150:153], v[196:199], v[4:7]
	v_mfma_f32_16x16x32_bf16 v[0:3], v[158:161], v[196:199], v[0:3]
	s_setprio 0
	s_barrier
	s_add_i32 s61, 0, 0x18000
	s_add_i32 s68, 0, 0x1c000
	v_add_u32_e32 v142, s61, v176
	v_add_u32_e32 v158, s68, v176
	ds_read_b128 v[130:133], v142
	ds_read_b128 v[134:137], v142 offset:1024
	ds_read_b128 v[138:141], v142 offset:2048
	ds_read_b128 v[142:145], v142 offset:3072
	ds_read_b128 v[146:149], v158
	ds_read_b128 v[150:153], v158 offset:1024
	ds_read_b128 v[154:157], v158 offset:2048
	ds_read_b128 v[158:161], v158 offset:3072
	s_add_u32 s64, s26, 0x40000
	v_mov_b32_e32 v200, v175
	s_addc_u32 s65, s27, 0
	s_mov_b32 m0, s39
	ds_read_b128 v[162:165], v179 offset:32768
	ds_read_b128 v[166:169], v179 offset:33792
	ds_read_b128 v[170:173], v179 offset:34816
	ds_read_b128 v[180:183], v179 offset:35840
	ds_read_b128 v[184:187], v179 offset:36864
	ds_read_b128 v[188:191], v179 offset:37888
	ds_read_b128 v[192:195], v179 offset:38912
	ds_read_b128 v[196:199], v179 offset:39936
	s_nop 0
	global_load_lds_dwordx4 v200, s[64:65]
	s_add_u32 s64, s26, 0x60000
	s_addc_u32 s65, s27, 0
	s_mov_b32 m0, s40
	s_nop 0
	global_load_lds_dwordx4 v175, s[64:65]
	s_waitcnt vmcnt(8)
	s_waitcnt lgkmcnt(0)
	s_barrier
	s_setprio 3
	v_mfma_f32_16x16x32_bf16 v[124:127], v[130:133], v[162:165], v[124:127]
	v_mfma_f32_16x16x32_bf16 v[120:123], v[138:141], v[162:165], v[120:123]
	v_mfma_f32_16x16x32_bf16 v[108:111], v[130:133], v[170:173], v[108:111]
	v_mfma_f32_16x16x32_bf16 v[104:107], v[138:141], v[170:173], v[104:107]
	v_mfma_f32_16x16x32_bf16 v[92:95], v[130:133], v[184:187], v[92:95]
	v_mfma_f32_16x16x32_bf16 v[88:91], v[138:141], v[184:187], v[88:91]
	v_mfma_f32_16x16x32_bf16 v[76:79], v[130:133], v[192:195], v[76:79]
	v_mfma_f32_16x16x32_bf16 v[72:75], v[138:141], v[192:195], v[72:75]
	v_mfma_f32_16x16x32_bf16 v[124:127], v[134:137], v[166:169], v[124:127]
	v_mfma_f32_16x16x32_bf16 v[120:123], v[142:145], v[166:169], v[120:123]
	v_mfma_f32_16x16x32_bf16 v[108:111], v[134:137], v[180:183], v[108:111]
	v_mfma_f32_16x16x32_bf16 v[104:107], v[142:145], v[180:183], v[104:107]
	v_mfma_f32_16x16x32_bf16 v[92:95], v[134:137], v[188:191], v[92:95]
	v_mfma_f32_16x16x32_bf16 v[88:91], v[142:145], v[188:191], v[88:91]
	v_mfma_f32_16x16x32_bf16 v[76:79], v[134:137], v[196:199], v[76:79]
	v_mfma_f32_16x16x32_bf16 v[72:75], v[142:145], v[196:199], v[72:75]
	v_mfma_f32_16x16x32_bf16 v[116:119], v[146:149], v[162:165], v[116:119]
	v_mfma_f32_16x16x32_bf16 v[112:115], v[154:157], v[162:165], v[112:115]
	v_mfma_f32_16x16x32_bf16 v[100:103], v[146:149], v[170:173], v[100:103]
	v_mfma_f32_16x16x32_bf16 v[96:99], v[154:157], v[170:173], v[96:99]
	v_mfma_f32_16x16x32_bf16 v[84:87], v[146:149], v[184:187], v[84:87]
	v_mfma_f32_16x16x32_bf16 v[80:83], v[154:157], v[184:187], v[80:83]
	v_mfma_f32_16x16x32_bf16 v[68:71], v[146:149], v[192:195], v[68:71]
	v_mfma_f32_16x16x32_bf16 v[64:67], v[154:157], v[192:195], v[64:67]
	v_mfma_f32_16x16x32_bf16 v[116:119], v[150:153], v[166:169], v[116:119]
	v_mfma_f32_16x16x32_bf16 v[112:115], v[158:161], v[166:169], v[112:115]
	v_mfma_f32_16x16x32_bf16 v[100:103], v[150:153], v[180:183], v[100:103]
	v_mfma_f32_16x16x32_bf16 v[96:99], v[158:161], v[180:183], v[96:99]
	v_mfma_f32_16x16x32_bf16 v[84:87], v[150:153], v[188:191], v[84:87]
	v_mfma_f32_16x16x32_bf16 v[80:83], v[158:161], v[188:191], v[80:83]
	v_mfma_f32_16x16x32_bf16 v[68:71], v[150:153], v[196:199], v[68:71]
	v_mfma_f32_16x16x32_bf16 v[64:67], v[158:161], v[196:199], v[64:67]
	s_setprio 0
	s_barrier
	s_add_u32 s64, s30, 0x80
	s_addc_u32 s65, s31, 0
	v_mov_b32_e32 v200, v174
	s_add_i32 s61, s61, s36
	ds_read_b128 v[162:165], v179 offset:49152
	ds_read_b128 v[166:169], v179 offset:50176
	ds_read_b128 v[170:173], v179 offset:51200
	ds_read_b128 v[180:183], v179 offset:52224
	ds_read_b128 v[184:187], v179 offset:53248
	ds_read_b128 v[188:191], v179 offset:54272
	ds_read_b128 v[192:195], v179 offset:55296
	ds_read_b128 v[196:199], v179 offset:56320
	s_mov_b32 m0, s61
	s_nop 0
	global_load_lds_dwordx4 v200, s[64:65]
	s_add_u32 s64, s30, 0x20080
	s_addc_u32 s65, s31, 0
	s_add_i32 m0, s61, 0x2000
	s_nop 0
	global_load_lds_dwordx4 v174, s[64:65]
	s_add_u32 s64, s30, 0x40080
	s_addc_u32 s65, s31, 0
	s_add_i32 s61, s68, s36
	s_mov_b32 m0, s61
	s_add_u32 s30, s30, 0x60080
	global_load_lds_dwordx4 v174, s[64:65]
	s_addc_u32 s31, s31, 0
	s_add_i32 m0, s61, 0x2000
	s_add_u32 s26, s26, 0x20080
	global_load_lds_dwordx4 v174, s[30:31]
	s_mov_b32 m0, s48
	s_addc_u32 s27, s27, 0
	global_load_lds_dwordx4 v175, s[28:29]
	s_mov_b32 m0, s49
	s_nop 0
	global_load_lds_dwordx4 v175, s[26:27]
	s_waitcnt vmcnt(8)
	s_waitcnt lgkmcnt(0)
	s_barrier
	s_setprio 3
	v_mfma_f32_16x16x32_bf16 v[60:63], v[130:133], v[162:165], v[60:63]
	v_mfma_f32_16x16x32_bf16 v[56:59], v[138:141], v[162:165], v[56:59]
	v_mfma_f32_16x16x32_bf16 v[44:47], v[130:133], v[170:173], v[44:47]
	v_mfma_f32_16x16x32_bf16 v[40:43], v[138:141], v[170:173], v[40:43]
	v_mfma_f32_16x16x32_bf16 v[28:31], v[130:133], v[184:187], v[28:31]
	v_mfma_f32_16x16x32_bf16 v[24:27], v[138:141], v[184:187], v[24:27]
	v_mfma_f32_16x16x32_bf16 v[12:15], v[130:133], v[192:195], v[12:15]
	v_mfma_f32_16x16x32_bf16 v[8:11], v[138:141], v[192:195], v[8:11]
	v_mfma_f32_16x16x32_bf16 v[60:63], v[134:137], v[166:169], v[60:63]
	v_mfma_f32_16x16x32_bf16 v[56:59], v[142:145], v[166:169], v[56:59]
	v_mfma_f32_16x16x32_bf16 v[44:47], v[134:137], v[180:183], v[44:47]
	v_mfma_f32_16x16x32_bf16 v[40:43], v[142:145], v[180:183], v[40:43]
	v_mfma_f32_16x16x32_bf16 v[28:31], v[134:137], v[188:191], v[28:31]
	v_mfma_f32_16x16x32_bf16 v[24:27], v[142:145], v[188:191], v[24:27]
	v_mfma_f32_16x16x32_bf16 v[12:15], v[134:137], v[196:199], v[12:15]
	v_mfma_f32_16x16x32_bf16 v[8:11], v[142:145], v[196:199], v[8:11]
	v_mfma_f32_16x16x32_bf16 v[52:55], v[146:149], v[162:165], v[52:55]
	v_mfma_f32_16x16x32_bf16 v[48:51], v[154:157], v[162:165], v[48:51]
	v_mfma_f32_16x16x32_bf16 v[36:39], v[146:149], v[170:173], v[36:39]
	v_mfma_f32_16x16x32_bf16 v[32:35], v[154:157], v[170:173], v[32:35]
	v_mfma_f32_16x16x32_bf16 v[20:23], v[146:149], v[184:187], v[20:23]
	v_mfma_f32_16x16x32_bf16 v[16:19], v[154:157], v[184:187], v[16:19]
	v_mfma_f32_16x16x32_bf16 v[4:7], v[146:149], v[192:195], v[4:7]
	v_mfma_f32_16x16x32_bf16 v[0:3], v[154:157], v[192:195], v[0:3]
	v_mfma_f32_16x16x32_bf16 v[52:55], v[150:153], v[166:169], v[52:55]
	s_add_i32 s60, s60, 2
	v_mfma_f32_16x16x32_bf16 v[48:51], v[158:161], v[166:169], v[48:51]
	s_add_u32 s15, s15, 0x100
	v_mfma_f32_16x16x32_bf16 v[36:39], v[150:153], v[180:183], v[36:39]
	s_addc_u32 s17, s17, 0
	v_mfma_f32_16x16x32_bf16 v[32:35], v[158:161], v[180:183], v[32:35]
	s_add_u32 s24, s24, 0x100
	v_mfma_f32_16x16x32_bf16 v[20:23], v[150:153], v[188:191], v[20:23]
	s_addc_u32 s25, s25, 0
	v_mfma_f32_16x16x32_bf16 v[16:19], v[158:161], v[188:191], v[16:19]
	s_cmp_gt_u32 s60, 13
	v_mfma_f32_16x16x32_bf16 v[4:7], v[150:153], v[196:199], v[4:7]
	v_mfma_f32_16x16x32_bf16 v[0:3], v[158:161], v[196:199], v[0:3]
	s_setprio 0
	s_barrier
	s_cbranch_scc0 .LBB0_725
	s_and_b64 vcc, exec, s[10:11]
	s_cbranch_vccz .LBB0_728
	s_barrier

.LBB0_1124:
	ds_read_b128 v[144:147], v137
	ds_read_b128 v[148:151], v137 offset:1024
	ds_read_b128 v[152:155], v137 offset:2048
	ds_read_b128 v[156:159], v137 offset:3072
	ds_read_b128 v[160:163], v138
	ds_read_b128 v[164:167], v138 offset:1024
	ds_read_b128 v[168:171], v138 offset:2048
	ds_read_b128 v[172:175], v138 offset:3072
	s_cmp_eq_u32 s70, 4
	s_cselect_b64 vcc, -1, 0
	s_and_b64 s[22:23], vcc, exec
	s_cselect_b32 s26, s8, s68
	s_cselect_b32 s27, s9, s69
	s_cselect_b32 s24, s20, s14
	s_cselect_b32 s25, s21, s65
	s_add_u32 s22, s26, 0x80
	s_addc_u32 s23, s27, 0
	s_add_u32 s72, s68, 0xffffff80
	s_addc_u32 s73, s69, -1
	v_mov_b32_e32 v132, v130
	s_mov_b32 m0, s49
	ds_read_b128 v[176:179], v139
	ds_read_b128 v[180:183], v139 offset:1024
	ds_read_b128 v[184:187], v139 offset:2048
	ds_read_b128 v[188:191], v139 offset:3072
	ds_read_b128 v[192:195], v139 offset:4096
	ds_read_b128 v[196:199], v139 offset:5120
	ds_read_b128 v[200:203], v139 offset:6144
	ds_read_b128 v[204:207], v139 offset:7168
	s_mov_b64 s[74:75], s[72:73]
	s_nop 0
	global_load_lds_dwordx4 v132, s[74:75]
	s_mov_b32 m0, s51
	s_nop 0
	global_load_lds_dwordx4 v131, s[72:73]
	s_waitcnt vmcnt(8)
	s_waitcnt lgkmcnt(0)
	s_barrier
	s_setprio 3
	v_mfma_f32_16x16x128_f8f6f4 v[124:127], v[144:151], v[176:183], v[124:127]
	v_mfma_f32_16x16x128_f8f6f4 v[116:119], v[152:159], v[176:183], v[116:119]
	v_mfma_f32_16x16x128_f8f6f4 v[108:111], v[144:151], v[184:191], v[108:111]
	v_mfma_f32_16x16x128_f8f6f4 v[100:103], v[152:159], v[184:191], v[100:103]
	v_mfma_f32_16x16x128_f8f6f4 v[92:95], v[144:151], v[192:199], v[92:95]
	v_mfma_f32_16x16x128_f8f6f4 v[84:87], v[152:159], v[192:199], v[84:87]
	v_mfma_f32_16x16x128_f8f6f4 v[76:79], v[144:151], v[200:207], v[76:79]
	v_mfma_f32_16x16x128_f8f6f4 v[68:71], v[152:159], v[200:207], v[68:71]
	v_mfma_f32_16x16x128_f8f6f4 v[120:123], v[160:167], v[176:183], v[120:123]
	v_mfma_f32_16x16x128_f8f6f4 v[112:115], v[168:175], v[176:183], v[112:115]
	v_mfma_f32_16x16x128_f8f6f4 v[104:107], v[160:167], v[184:191], v[104:107]
	v_mfma_f32_16x16x128_f8f6f4 v[96:99], v[168:175], v[184:191], v[96:99]
	v_mfma_f32_16x16x128_f8f6f4 v[88:91], v[160:167], v[192:199], v[88:91]
	v_mfma_f32_16x16x128_f8f6f4 v[80:83], v[168:175], v[192:199], v[80:83]
	v_mfma_f32_16x16x128_f8f6f4 v[72:75], v[160:167], v[200:207], v[72:75]
	v_mfma_f32_16x16x128_f8f6f4 v[64:67], v[168:175], v[200:207], v[64:67]
	s_setprio 0
	s_barrier
	v_mov_b32_e32 v132, v134
	s_mov_b64 s[72:73], s[24:25]
	s_mov_b32 m0, s52
	ds_read_b128 v[176:179], v139 offset:16384
	ds_read_b128 v[180:183], v139 offset:17408
	ds_read_b128 v[184:187], v139 offset:18432
	ds_read_b128 v[188:191], v139 offset:19456
	ds_read_b128 v[192:195], v139 offset:20480
	ds_read_b128 v[196:199], v139 offset:21504
	ds_read_b128 v[200:203], v139 offset:22528
	ds_read_b128 v[204:207], v139 offset:23552
	s_nop 0
	global_load_lds_dwordx4 v132, s[72:73]
	s_add_u32 s72, s24, 0x10000
	s_addc_u32 s73, s25, 0
	s_add_i32 m0, s52, 0x2000
	s_nop 0
	global_load_lds_dwordx4 v134, s[72:73]
	s_add_u32 s72, s24, 0x20000
	s_addc_u32 s73, s25, 0
	s_add_i32 s71, s48, s35
	s_mov_b32 m0, s71
	s_nop 0
	global_load_lds_dwordx4 v134, s[72:73]
	s_add_u32 s72, s24, 0x30000
	s_addc_u32 s73, s25, 0
	s_add_i32 m0, s71, 0x2000
	s_nop 0
	global_load_lds_dwordx4 v134, s[72:73]
	v_cndmask_b32_e32 v132, v128, v141, vcc
	v_lshlrev_b32_e32 v133, 10, v132
	v_and_or_b32 v133, v133, s37, v135
	s_mov_b64 s[72:73], s[26:27]
	s_mov_b32 m0, s36
	s_nop 0
	global_load_lds_dwordx4 v133, s[72:73]
	v_cndmask_b32_e32 v143, v129, v142, vcc
	v_lshlrev_b32_e32 v208, 10, v143
	v_and_or_b32 v208, v208, s37, v135
	s_mov_b64 s[72:73], s[26:27]
	s_mov_b32 m0, s38
	s_nop 0
	global_load_lds_dwordx4 v208, s[72:73]
	s_waitcnt vmcnt(8)
	s_waitcnt lgkmcnt(0)
	s_barrier
	s_setprio 3
	v_mfma_f32_16x16x128_f8f6f4 v[60:63], v[144:151], v[176:183], v[60:63]
	v_mfma_f32_16x16x128_f8f6f4 v[52:55], v[152:159], v[176:183], v[52:55]
	v_mfma_f32_16x16x128_f8f6f4 v[44:47], v[144:151], v[184:191], v[44:47]
	v_mfma_f32_16x16x128_f8f6f4 v[36:39], v[152:159], v[184:191], v[36:39]
	v_mfma_f32_16x16x128_f8f6f4 v[28:31], v[144:151], v[192:199], v[28:31]
	v_mfma_f32_16x16x128_f8f6f4 v[20:23], v[152:159], v[192:199], v[20:23]
	v_mfma_f32_16x16x128_f8f6f4 v[12:15], v[144:151], v[200:207], v[12:15]
	v_mfma_f32_16x16x128_f8f6f4 v[4:7], v[152:159], v[200:207], v[4:7]
	v_mfma_f32_16x16x128_f8f6f4 v[56:59], v[160:167], v[176:183], v[56:59]
	v_mfma_f32_16x16x128_f8f6f4 v[48:51], v[168:175], v[176:183], v[48:51]
	v_mfma_f32_16x16x128_f8f6f4 v[40:43], v[160:167], v[184:191], v[40:43]
	v_mfma_f32_16x16x128_f8f6f4 v[32:35], v[168:175], v[184:191], v[32:35]
	v_mfma_f32_16x16x128_f8f6f4 v[24:27], v[160:167], v[192:199], v[24:27]
	v_mfma_f32_16x16x128_f8f6f4 v[16:19], v[168:175], v[192:199], v[16:19]
	v_mfma_f32_16x16x128_f8f6f4 v[8:11], v[160:167], v[200:207], v[8:11]
	v_mfma_f32_16x16x128_f8f6f4 v[0:3], v[168:175], v[200:207], v[0:3]
	s_setprio 0
	s_barrier
	s_add_i32 s71, 0, 0x18000
	s_add_i32 s74, 0, 0x1c000
	v_add_u32_e32 v156, s71, v136
	v_add_u32_e32 v172, s74, v136
	ds_read_b128 v[144:147], v156
	ds_read_b128 v[148:151], v156 offset:1024
	ds_read_b128 v[152:155], v156 offset:2048
	ds_read_b128 v[156:159], v156 offset:3072
	ds_read_b128 v[160:163], v172
	ds_read_b128 v[164:167], v172 offset:1024
	ds_read_b128 v[168:171], v172 offset:2048
	ds_read_b128 v[172:175], v172 offset:3072
	v_bfe_u32 v132, v132, 16, 16
	v_lshl_or_b32 v132, v132, 10, v135
	s_mov_b32 m0, s39
	ds_read_b128 v[176:179], v139 offset:32768
	ds_read_b128 v[180:183], v139 offset:33792
	ds_read_b128 v[184:187], v139 offset:34816
	ds_read_b128 v[188:191], v139 offset:35840
	ds_read_b128 v[192:195], v139 offset:36864
	ds_read_b128 v[196:199], v139 offset:37888
	ds_read_b128 v[200:203], v139 offset:38912
	ds_read_b128 v[204:207], v139 offset:39936
	s_mov_b64 s[72:73], s[26:27]
	s_nop 0
	global_load_lds_dwordx4 v132, s[72:73]
	v_bfe_u32 v132, v143, 16, 16
	v_lshl_or_b32 v132, v132, 10, v135
	s_mov_b32 m0, s40
	s_nop 0
	global_load_lds_dwordx4 v132, s[26:27]
	s_waitcnt vmcnt(8)
	s_waitcnt lgkmcnt(0)
	s_barrier
	s_setprio 3
	v_mfma_f32_16x16x128_f8f6f4 v[124:127], v[144:151], v[176:183], v[124:127]
	v_mfma_f32_16x16x128_f8f6f4 v[116:119], v[152:159], v[176:183], v[116:119]
	v_mfma_f32_16x16x128_f8f6f4 v[108:111], v[144:151], v[184:191], v[108:111]
	v_mfma_f32_16x16x128_f8f6f4 v[100:103], v[152:159], v[184:191], v[100:103]
	v_mfma_f32_16x16x128_f8f6f4 v[92:95], v[144:151], v[192:199], v[92:95]
	v_mfma_f32_16x16x128_f8f6f4 v[84:87], v[152:159], v[192:199], v[84:87]
	v_mfma_f32_16x16x128_f8f6f4 v[76:79], v[144:151], v[200:207], v[76:79]
	v_mfma_f32_16x16x128_f8f6f4 v[68:71], v[152:159], v[200:207], v[68:71]
	v_mfma_f32_16x16x128_f8f6f4 v[120:123], v[160:167], v[176:183], v[120:123]
	v_mfma_f32_16x16x128_f8f6f4 v[112:115], v[168:175], v[176:183], v[112:115]
	v_mfma_f32_16x16x128_f8f6f4 v[104:107], v[160:167], v[184:191], v[104:107]
	v_mfma_f32_16x16x128_f8f6f4 v[96:99], v[168:175], v[184:191], v[96:99]
	v_mfma_f32_16x16x128_f8f6f4 v[88:91], v[160:167], v[192:199], v[88:91]
	v_mfma_f32_16x16x128_f8f6f4 v[80:83], v[168:175], v[192:199], v[80:83]
	v_mfma_f32_16x16x128_f8f6f4 v[72:75], v[160:167], v[200:207], v[72:75]
	v_mfma_f32_16x16x128_f8f6f4 v[64:67], v[168:175], v[200:207], v[64:67]
	s_setprio 0
	s_barrier
	s_add_u32 s26, s24, 0x80
	s_addc_u32 s27, s25, 0
	v_mov_b32_e32 v132, v134
	s_add_i32 s71, s71, s35
	ds_read_b128 v[176:179], v139 offset:49152
	ds_read_b128 v[180:183], v139 offset:50176
	ds_read_b128 v[184:187], v139 offset:51200
	ds_read_b128 v[188:191], v139 offset:52224
	ds_read_b128 v[192:195], v139 offset:53248
	ds_read_b128 v[196:199], v139 offset:54272
	ds_read_b128 v[200:203], v139 offset:55296
	ds_read_b128 v[204:207], v139 offset:56320
	s_mov_b32 m0, s71
	s_nop 0
	global_load_lds_dwordx4 v132, s[26:27]
	s_add_u32 s26, s24, 0x10080
	s_addc_u32 s27, s25, 0
	s_add_i32 m0, s71, 0x2000
	s_nop 0
	global_load_lds_dwordx4 v134, s[26:27]
	s_add_u32 s26, s24, 0x20080
	s_addc_u32 s27, s25, 0
	s_add_i32 s71, s74, s35
	s_mov_b32 m0, s71
	s_add_u32 s24, s24, 0x30080
	s_addc_u32 s25, s25, 0
	global_load_lds_dwordx4 v134, s[26:27]
	s_add_i32 m0, s71, 0x2000
	s_nop 0
	global_load_lds_dwordx4 v134, s[24:25]
	s_mov_b64 s[24:25], s[22:23]
	s_mov_b32 m0, s43
	s_nop 0
	global_load_lds_dwordx4 v133, s[24:25]
	s_mov_b32 m0, s44
	s_nop 0
	global_load_lds_dwordx4 v208, s[22:23]
	s_waitcnt vmcnt(8)
	s_waitcnt lgkmcnt(0)
	s_barrier
	s_setprio 3
	v_mfma_f32_16x16x128_f8f6f4 v[60:63], v[144:151], v[176:183], v[60:63]
	v_mfma_f32_16x16x128_f8f6f4 v[52:55], v[152:159], v[176:183], v[52:55]
	v_mfma_f32_16x16x128_f8f6f4 v[44:47], v[144:151], v[184:191], v[44:47]
	v_mfma_f32_16x16x128_f8f6f4 v[36:39], v[152:159], v[184:191], v[36:39]
	v_mfma_f32_16x16x128_f8f6f4 v[28:31], v[144:151], v[192:199], v[28:31]
	v_mfma_f32_16x16x128_f8f6f4 v[20:23], v[152:159], v[192:199], v[20:23]
	v_mfma_f32_16x16x128_f8f6f4 v[12:15], v[144:151], v[200:207], v[12:15]
	v_mfma_f32_16x16x128_f8f6f4 v[4:7], v[152:159], v[200:207], v[4:7]
	v_mfma_f32_16x16x128_f8f6f4 v[56:59], v[160:167], v[176:183], v[56:59]
	s_add_i32 s70, s70, 2
	v_mfma_f32_16x16x128_f8f6f4 v[48:51], v[168:175], v[176:183], v[48:51]
	s_add_u32 s14, s14, 0x100
	v_mfma_f32_16x16x128_f8f6f4 v[40:43], v[160:167], v[184:191], v[40:43]
	s_addc_u32 s65, s65, 0
	v_mfma_f32_16x16x128_f8f6f4 v[32:35], v[168:175], v[184:191], v[32:35]
	s_add_u32 s68, s68, 0x100
	v_mfma_f32_16x16x128_f8f6f4 v[24:27], v[160:167], v[192:199], v[24:27]
	s_addc_u32 s69, s69, 0
	v_mfma_f32_16x16x128_f8f6f4 v[16:19], v[168:175], v[192:199], v[16:19]
	s_cmp_gt_u32 s70, 5
	v_mfma_f32_16x16x128_f8f6f4 v[8:11], v[160:167], v[200:207], v[8:11]
	v_mfma_f32_16x16x128_f8f6f4 v[0:3], v[168:175], v[200:207], v[0:3]
	s_setprio 0
	s_barrier
	s_cbranch_scc0 .LBB0_1124
	s_and_b64 vcc, exec, s[18:19]
	s_cbranch_vccz .LBB0_1127
	s_barrier

.LBB0_1286:
	ds_read_b128 v[72:75], v67
	ds_read_b128 v[76:79], v67 offset:1024
	ds_read_b128 v[80:83], v67 offset:2048
	ds_read_b128 v[84:87], v67 offset:3072
	ds_read_b128 v[88:91], v68
	ds_read_b128 v[92:95], v68 offset:1024
	ds_read_b128 v[96:99], v68 offset:2048
	ds_read_b128 v[100:103], v68 offset:3072
	s_cmp_eq_u32 s37, 4
	s_cselect_b32 s16, s8, s35
	s_cselect_b32 s17, s9, s36
	s_cselect_b32 s14, s0, s31
	s_cselect_b32 s15, s1, s34
	s_add_u32 s4, s16, 0x80
	s_addc_u32 s5, s17, 0
	ds_read_b128 v[104:107], v69
	ds_read_b128 v[108:111], v69 offset:1024
	ds_read_b128 v[112:115], v69 offset:2048
	ds_read_b128 v[116:119], v69 offset:3072
	ds_read_b128 v[120:123], v69 offset:4096
	ds_read_b128 v[124:127], v69 offset:5120
	ds_read_b128 v[128:131], v69 offset:6144
	ds_read_b128 v[132:135], v69 offset:7168
	s_waitcnt vmcnt(6)
	s_waitcnt lgkmcnt(0)
	s_barrier
	s_setprio 3
	v_mfma_f32_16x16x128_f8f6f4 v[60:63], v[72:79], v[104:111], v[60:63]
	v_mfma_f32_16x16x128_f8f6f4 v[52:55], v[80:87], v[104:111], v[52:55]
	v_mfma_f32_16x16x128_f8f6f4 v[44:47], v[72:79], v[112:119], v[44:47]
	v_mfma_f32_16x16x128_f8f6f4 v[36:39], v[80:87], v[112:119], v[36:39]
	v_mfma_f32_16x16x128_f8f6f4 v[28:31], v[72:79], v[120:127], v[28:31]
	v_mfma_f32_16x16x128_f8f6f4 v[20:23], v[80:87], v[120:127], v[20:23]
	v_mfma_f32_16x16x128_f8f6f4 v[12:15], v[72:79], v[128:135], v[12:15]
	v_mfma_f32_16x16x128_f8f6f4 v[136:139], v[80:87], v[128:135], v[4:7]
	v_mfma_f32_16x16x128_f8f6f4 v[56:59], v[88:95], v[104:111], v[56:59]
	v_mfma_f32_16x16x128_f8f6f4 v[48:51], v[96:103], v[104:111], v[48:51]
	v_mfma_f32_16x16x128_f8f6f4 v[40:43], v[88:95], v[112:119], v[40:43]
	v_mfma_f32_16x16x128_f8f6f4 v[32:35], v[96:103], v[112:119], v[32:35]
	v_mfma_f32_16x16x128_f8f6f4 v[24:27], v[88:95], v[120:127], v[24:27]
	v_mfma_f32_16x16x128_f8f6f4 v[16:19], v[96:103], v[120:127], v[16:19]
	v_mfma_f32_16x16x128_f8f6f4 v[8:11], v[88:95], v[128:135], v[8:11]
	v_mfma_f32_16x16x128_f8f6f4 v[128:131], v[96:103], v[128:135], v[0:3]
	s_setprio 0
	s_barrier
	s_nop 4
	s_mov_b64 s[48:49], s[14:15]
	s_mov_b32 m0, s38
	s_nop 0
	global_load_lds_dwordx4 v64, s[48:49]
	s_add_u32 s48, s14, 0x10000
	s_addc_u32 s49, s15, 0
	s_mov_b32 m0, s39
	s_nop 0
	global_load_lds_dwordx4 v64, s[48:49]
	s_add_u32 s48, s14, 0x20000
	s_addc_u32 s49, s15, 0
	s_mov_b32 m0, s40
	s_nop 0
	global_load_lds_dwordx4 v64, s[48:49]
	s_add_u32 s48, s14, 0x30000
	s_addc_u32 s49, s15, 0
	s_mov_b32 m0, s41
	s_nop 0
	global_load_lds_dwordx4 v64, s[48:49]
	s_mov_b64 s[48:49], s[16:17]
	s_mov_b32 m0, s23
	s_nop 0
	global_load_lds_dwordx4 v65, s[48:49]
	s_mov_b32 m0, s25
	s_nop 0
	global_load_lds_dwordx4 v66, s[16:17]
	s_waitcnt vmcnt(6)
	s_waitcnt lgkmcnt(0)
	s_barrier
	s_barrier
	ds_read_b128 v[0:3], v70
	ds_read_b128 v[4:7], v70 offset:1024
	ds_read_b128 v[72:75], v70 offset:2048
	ds_read_b128 v[76:79], v70 offset:3072
	ds_read_b128 v[80:83], v71
	ds_read_b128 v[84:87], v71 offset:1024
	ds_read_b128 v[88:91], v71 offset:2048
	ds_read_b128 v[92:95], v71 offset:3072
	ds_read_b128 v[96:99], v69 offset:32768
	ds_read_b128 v[100:103], v69 offset:33792
	ds_read_b128 v[104:107], v69 offset:34816
	ds_read_b128 v[108:111], v69 offset:35840
	ds_read_b128 v[112:115], v69 offset:36864
	ds_read_b128 v[116:119], v69 offset:37888
	ds_read_b128 v[120:123], v69 offset:38912
	ds_read_b128 v[124:127], v69 offset:39936
	s_waitcnt vmcnt(6)
	s_waitcnt lgkmcnt(0)
	s_barrier
	s_setprio 3
	v_mfma_f32_16x16x128_f8f6f4 v[60:63], v[0:7], v[96:103], v[60:63]
	v_mfma_f32_16x16x128_f8f6f4 v[52:55], v[72:79], v[96:103], v[52:55]
	v_mfma_f32_16x16x128_f8f6f4 v[44:47], v[0:7], v[104:111], v[44:47]
	v_mfma_f32_16x16x128_f8f6f4 v[36:39], v[72:79], v[104:111], v[36:39]
	v_mfma_f32_16x16x128_f8f6f4 v[28:31], v[0:7], v[112:119], v[28:31]
	v_mfma_f32_16x16x128_f8f6f4 v[20:23], v[72:79], v[112:119], v[20:23]
	v_mfma_f32_16x16x128_f8f6f4 v[12:15], v[0:7], v[120:127], v[12:15]
	v_mfma_f32_16x16x128_f8f6f4 v[4:7], v[72:79], v[120:127], v[136:139]
	v_mfma_f32_16x16x128_f8f6f4 v[56:59], v[80:87], v[96:103], v[56:59]
	s_add_u32 s16, s14, 0x80
	s_addc_u32 s17, s15, 0
	v_mfma_f32_16x16x128_f8f6f4 v[48:51], v[88:95], v[96:103], v[48:51]
	v_mfma_f32_16x16x128_f8f6f4 v[40:43], v[80:87], v[104:111], v[40:43]
	v_mfma_f32_16x16x128_f8f6f4 v[32:35], v[88:95], v[104:111], v[32:35]
	v_mfma_f32_16x16x128_f8f6f4 v[24:27], v[80:87], v[112:119], v[24:27]
	v_mfma_f32_16x16x128_f8f6f4 v[16:19], v[88:95], v[112:119], v[16:19]
	v_mfma_f32_16x16x128_f8f6f4 v[8:11], v[80:87], v[120:127], v[8:11]
	v_mfma_f32_16x16x128_f8f6f4 v[0:3], v[88:95], v[120:127], v[128:131]
	s_setprio 0
	s_barrier
	s_mov_b32 m0, s42
	s_nop 0
	global_load_lds_dwordx4 v64, s[16:17]
	s_add_u32 s16, s14, 0x10080
	s_addc_u32 s17, s15, 0
	s_mov_b32 m0, s43
	s_nop 0
	global_load_lds_dwordx4 v64, s[16:17]
	s_add_u32 s16, s14, 0x20080
	s_addc_u32 s17, s15, 0
	s_mov_b32 m0, s44
	s_add_u32 s14, s14, 0x30080
	global_load_lds_dwordx4 v64, s[16:17]
	s_addc_u32 s15, s15, 0
	s_mov_b32 m0, s45
	s_nop 0
	global_load_lds_dwordx4 v64, s[14:15]
	s_mov_b64 s[14:15], s[4:5]
	s_mov_b32 m0, s26
	s_nop 0
	global_load_lds_dwordx4 v65, s[14:15]
	s_mov_b32 m0, s27
	s_nop 0
	global_load_lds_dwordx4 v66, s[4:5]
	s_add_i32 s37, s37, 2
	s_add_u32 s31, s31, 0x100
	s_addc_u32 s34, s34, 0
	s_add_u32 s35, s35, 0x100
	s_addc_u32 s36, s36, 0
	s_cmp_gt_u32 s37, 5
	s_waitcnt vmcnt(6)
	s_waitcnt lgkmcnt(0)
	s_barrier
	s_barrier
	s_cbranch_scc0 .LBB0_1286
	s_cmpk_lt_u32 s22, 0x100
	s_cbranch_scc0 .LBB0_1289
	s_barrier

.LBB0_1769:
	ds_read_b128 v[56:59], v155
	ds_read_b128 v[60:63], v155 offset:1024
	ds_read_b128 v[68:71], v155 offset:2048
	ds_read_b128 v[76:79], v155 offset:3072
	ds_read_b128 v[146:149], v156
	ds_read_b128 v[160:163], v156 offset:1024
	ds_read_b128 v[164:167], v156 offset:2048
	ds_read_b128 v[168:171], v156 offset:3072
	s_add_u32 s69, s6, 0xfffa0080
	s_addc_u32 s70, s7, -1
	s_cmp_eq_u32 s53, 12
	s_cselect_b32 s71, s61, s70
	s_cselect_b32 s70, s60, s69
	s_cselect_b32 s74, s64, s5
	s_cselect_b32 s75, s65, s51
	s_add_u32 s72, s70, 0x80
	s_addc_u32 s73, s71, 0
	s_add_u32 s80, s6, 0xfffe0000
	v_mov_b32_e32 v150, v153
	s_addc_u32 s81, s7, -1
	ds_read_b128 v[172:175], v157
	ds_read_b128 v[176:179], v157 offset:1024
	ds_read_b128 v[180:183], v157 offset:2048
	ds_read_b128 v[184:187], v157 offset:3072
	ds_read_b128 v[188:191], v157 offset:4096
	ds_read_b128 v[192:195], v157 offset:5120
	ds_read_b128 v[196:199], v157 offset:6144
	ds_read_b128 v[200:203], v157 offset:7168
	s_add_i32 m0, s25, 0xc000
	s_nop 0
	global_load_lds_dwordx4 v150, s[80:81]
	s_mov_b64 s[80:81], s[6:7]
	s_add_i32 m0, s25, 0xe000
	s_nop 0
	global_load_lds_dwordx4 v153, s[80:81]
	s_waitcnt vmcnt(8)
	s_waitcnt lgkmcnt(0)
	s_barrier
	s_setprio 3
	v_mfma_f32_16x16x32_bf16 v[140:143], v[56:59], v[172:175], v[140:143]
	v_mfma_f32_16x16x32_bf16 v[136:139], v[68:71], v[172:175], v[136:139]
	v_mfma_f32_16x16x32_bf16 v[124:127], v[56:59], v[180:183], v[124:127]
	v_mfma_f32_16x16x32_bf16 v[120:123], v[68:71], v[180:183], v[120:123]
	v_mfma_f32_16x16x32_bf16 v[108:111], v[56:59], v[188:191], v[108:111]
	v_mfma_f32_16x16x32_bf16 v[104:107], v[68:71], v[188:191], v[104:107]
	v_mfma_f32_16x16x32_bf16 v[92:95], v[56:59], v[196:199], v[92:95]
	v_mfma_f32_16x16x32_bf16 v[88:91], v[68:71], v[196:199], v[88:91]
	v_mfma_f32_16x16x32_bf16 v[140:143], v[60:63], v[176:179], v[140:143]
	v_mfma_f32_16x16x32_bf16 v[136:139], v[76:79], v[176:179], v[136:139]
	v_mfma_f32_16x16x32_bf16 v[124:127], v[60:63], v[184:187], v[124:127]
	v_mfma_f32_16x16x32_bf16 v[120:123], v[76:79], v[184:187], v[120:123]
	v_mfma_f32_16x16x32_bf16 v[108:111], v[60:63], v[192:195], v[108:111]
	v_mfma_f32_16x16x32_bf16 v[104:107], v[76:79], v[192:195], v[104:107]
	v_mfma_f32_16x16x32_bf16 v[92:95], v[60:63], v[200:203], v[92:95]
	v_mfma_f32_16x16x32_bf16 v[88:91], v[76:79], v[200:203], v[88:91]
	v_mfma_f32_16x16x32_bf16 v[132:135], v[146:149], v[172:175], v[132:135]
	v_mfma_f32_16x16x32_bf16 v[128:131], v[164:167], v[172:175], v[128:131]
	v_mfma_f32_16x16x32_bf16 v[116:119], v[146:149], v[180:183], v[116:119]
	v_mfma_f32_16x16x32_bf16 v[112:115], v[164:167], v[180:183], v[112:115]
	v_mfma_f32_16x16x32_bf16 v[100:103], v[146:149], v[188:191], v[100:103]
	v_mfma_f32_16x16x32_bf16 v[96:99], v[164:167], v[188:191], v[96:99]
	v_mfma_f32_16x16x32_bf16 v[84:87], v[146:149], v[196:199], v[84:87]
	v_mfma_f32_16x16x32_bf16 v[80:83], v[164:167], v[196:199], v[80:83]
	v_mfma_f32_16x16x32_bf16 v[132:135], v[160:163], v[176:179], v[132:135]
	v_mfma_f32_16x16x32_bf16 v[128:131], v[168:171], v[176:179], v[128:131]
	v_mfma_f32_16x16x32_bf16 v[116:119], v[160:163], v[184:187], v[116:119]
	v_mfma_f32_16x16x32_bf16 v[112:115], v[168:171], v[184:187], v[112:115]
	v_mfma_f32_16x16x32_bf16 v[100:103], v[160:163], v[192:195], v[100:103]
	v_mfma_f32_16x16x32_bf16 v[96:99], v[168:171], v[192:195], v[96:99]
	v_mfma_f32_16x16x32_bf16 v[84:87], v[160:163], v[200:203], v[84:87]
	v_mfma_f32_16x16x32_bf16 v[80:83], v[168:171], v[200:203], v[80:83]
	s_setprio 0
	s_barrier
	v_mov_b32_e32 v150, v152
	s_mov_b64 s[80:81], s[74:75]
	s_add_i32 s69, s49, s23
	ds_read_b128 v[172:175], v157 offset:16384
	ds_read_b128 v[176:179], v157 offset:17408
	ds_read_b128 v[180:183], v157 offset:18432
	ds_read_b128 v[184:187], v157 offset:19456
	ds_read_b128 v[188:191], v157 offset:20480
	ds_read_b128 v[192:195], v157 offset:21504
	ds_read_b128 v[196:199], v157 offset:22528
	ds_read_b128 v[200:203], v157 offset:23552
	s_mov_b32 m0, s69
	s_nop 0
	global_load_lds_dwordx4 v150, s[80:81]
	s_add_u32 s80, s74, 0x20000
	s_addc_u32 s81, s75, 0
	s_add_i32 m0, s69, 0x2000
	s_nop 0
	global_load_lds_dwordx4 v152, s[80:81]
	s_add_u32 s80, s74, 0x40000
	s_addc_u32 s81, s75, 0
	s_add_i32 s69, s77, s23
	s_mov_b32 m0, s69
	s_nop 0
	global_load_lds_dwordx4 v152, s[80:81]
	s_add_u32 s80, s74, 0x60000
	s_addc_u32 s81, s75, 0
	s_add_i32 m0, s69, 0x2000
	s_nop 0
	global_load_lds_dwordx4 v152, s[80:81]
	s_mov_b64 s[80:81], s[70:71]
	s_mov_b32 m0, s25
	s_nop 0
	global_load_lds_dwordx4 v153, s[80:81]
	s_add_u32 s80, s70, 0x20000
	s_addc_u32 s81, s71, 0
	s_mov_b32 m0, s27
	s_nop 0
	global_load_lds_dwordx4 v153, s[80:81]
	s_waitcnt vmcnt(8)
	s_waitcnt lgkmcnt(0)
	s_barrier
	s_setprio 3
	v_mfma_f32_16x16x32_bf16 v[72:75], v[56:59], v[172:175], v[72:75]
	v_mfma_f32_16x16x32_bf16 v[64:67], v[68:71], v[172:175], v[64:67]
	v_mfma_f32_16x16x32_bf16 v[44:47], v[56:59], v[180:183], v[44:47]
	v_mfma_f32_16x16x32_bf16 v[40:43], v[68:71], v[180:183], v[40:43]
	v_mfma_f32_16x16x32_bf16 v[28:31], v[56:59], v[188:191], v[28:31]
	v_mfma_f32_16x16x32_bf16 v[24:27], v[68:71], v[188:191], v[24:27]
	v_mfma_f32_16x16x32_bf16 v[12:15], v[56:59], v[196:199], v[12:15]
	v_mfma_f32_16x16x32_bf16 v[8:11], v[68:71], v[196:199], v[8:11]
	v_mfma_f32_16x16x32_bf16 v[72:75], v[60:63], v[176:179], v[72:75]
	v_mfma_f32_16x16x32_bf16 v[64:67], v[76:79], v[176:179], v[64:67]
	v_mfma_f32_16x16x32_bf16 v[44:47], v[60:63], v[184:187], v[44:47]
	v_mfma_f32_16x16x32_bf16 v[40:43], v[76:79], v[184:187], v[40:43]
	v_mfma_f32_16x16x32_bf16 v[28:31], v[60:63], v[192:195], v[28:31]
	v_mfma_f32_16x16x32_bf16 v[24:27], v[76:79], v[192:195], v[24:27]
	v_mfma_f32_16x16x32_bf16 v[12:15], v[60:63], v[200:203], v[12:15]
	v_mfma_f32_16x16x32_bf16 v[8:11], v[76:79], v[200:203], v[8:11]
	v_mfma_f32_16x16x32_bf16 v[52:55], v[146:149], v[172:175], v[52:55]
	v_mfma_f32_16x16x32_bf16 v[48:51], v[164:167], v[172:175], v[48:51]
	v_mfma_f32_16x16x32_bf16 v[36:39], v[146:149], v[180:183], v[36:39]
	v_mfma_f32_16x16x32_bf16 v[32:35], v[164:167], v[180:183], v[32:35]
	v_mfma_f32_16x16x32_bf16 v[20:23], v[146:149], v[188:191], v[20:23]
	v_mfma_f32_16x16x32_bf16 v[16:19], v[164:167], v[188:191], v[16:19]
	v_mfma_f32_16x16x32_bf16 v[4:7], v[146:149], v[196:199], v[4:7]
	v_mfma_f32_16x16x32_bf16 v[0:3], v[164:167], v[196:199], v[0:3]
	v_mfma_f32_16x16x32_bf16 v[52:55], v[160:163], v[176:179], v[52:55]
	v_mfma_f32_16x16x32_bf16 v[48:51], v[168:171], v[176:179], v[48:51]
	v_mfma_f32_16x16x32_bf16 v[36:39], v[160:163], v[184:187], v[36:39]
	v_mfma_f32_16x16x32_bf16 v[32:35], v[168:171], v[184:187], v[32:35]
	v_mfma_f32_16x16x32_bf16 v[20:23], v[160:163], v[192:195], v[20:23]
	v_mfma_f32_16x16x32_bf16 v[16:19], v[168:171], v[192:195], v[16:19]
	v_mfma_f32_16x16x32_bf16 v[4:7], v[160:163], v[200:203], v[4:7]
	v_mfma_f32_16x16x32_bf16 v[0:3], v[168:171], v[200:203], v[0:3]
	s_setprio 0
	s_barrier
	s_add_i32 s69, 0, 0x18000
	s_add_i32 s82, 0, 0x1c000
	v_add_u32_e32 v76, s69, v154
	v_add_u32_e32 v150, s82, v154
	ds_read_b128 v[56:59], v76
	ds_read_b128 v[60:63], v76 offset:1024
	ds_read_b128 v[68:71], v76 offset:2048
	ds_read_b128 v[76:79], v76 offset:3072
	ds_read_b128 v[146:149], v150
	ds_read_b128 v[160:163], v150 offset:1024
	ds_read_b128 v[164:167], v150 offset:2048
	ds_read_b128 v[168:171], v150 offset:3072
	s_add_u32 s80, s70, 0x40000
	v_mov_b32_e32 v150, v153
	s_addc_u32 s81, s71, 0
	s_mov_b32 m0, s29
	ds_read_b128 v[172:175], v157 offset:32768
	ds_read_b128 v[176:179], v157 offset:33792
	ds_read_b128 v[180:183], v157 offset:34816
	ds_read_b128 v[184:187], v157 offset:35840
	ds_read_b128 v[188:191], v157 offset:36864
	ds_read_b128 v[192:195], v157 offset:37888
	ds_read_b128 v[196:199], v157 offset:38912
	ds_read_b128 v[200:203], v157 offset:39936
	s_nop 0
	global_load_lds_dwordx4 v150, s[80:81]
	s_add_u32 s80, s70, 0x60000
	s_addc_u32 s81, s71, 0
	s_mov_b32 m0, s31
	s_nop 0
	global_load_lds_dwordx4 v153, s[80:81]
	s_waitcnt vmcnt(8)
	s_waitcnt lgkmcnt(0)
	s_barrier
	s_setprio 3
	v_mfma_f32_16x16x32_bf16 v[140:143], v[56:59], v[172:175], v[140:143]
	v_mfma_f32_16x16x32_bf16 v[136:139], v[68:71], v[172:175], v[136:139]
	v_mfma_f32_16x16x32_bf16 v[124:127], v[56:59], v[180:183], v[124:127]
	v_mfma_f32_16x16x32_bf16 v[120:123], v[68:71], v[180:183], v[120:123]
	v_mfma_f32_16x16x32_bf16 v[108:111], v[56:59], v[188:191], v[108:111]
	v_mfma_f32_16x16x32_bf16 v[104:107], v[68:71], v[188:191], v[104:107]
	v_mfma_f32_16x16x32_bf16 v[92:95], v[56:59], v[196:199], v[92:95]
	v_mfma_f32_16x16x32_bf16 v[88:91], v[68:71], v[196:199], v[88:91]
	v_mfma_f32_16x16x32_bf16 v[140:143], v[60:63], v[176:179], v[140:143]
	v_mfma_f32_16x16x32_bf16 v[136:139], v[76:79], v[176:179], v[136:139]
	v_mfma_f32_16x16x32_bf16 v[124:127], v[60:63], v[184:187], v[124:127]
	v_mfma_f32_16x16x32_bf16 v[120:123], v[76:79], v[184:187], v[120:123]
	v_mfma_f32_16x16x32_bf16 v[108:111], v[60:63], v[192:195], v[108:111]
	v_mfma_f32_16x16x32_bf16 v[104:107], v[76:79], v[192:195], v[104:107]
	v_mfma_f32_16x16x32_bf16 v[92:95], v[60:63], v[200:203], v[92:95]
	v_mfma_f32_16x16x32_bf16 v[88:91], v[76:79], v[200:203], v[88:91]
	v_mfma_f32_16x16x32_bf16 v[132:135], v[146:149], v[172:175], v[132:135]
	v_mfma_f32_16x16x32_bf16 v[128:131], v[164:167], v[172:175], v[128:131]
	v_mfma_f32_16x16x32_bf16 v[116:119], v[146:149], v[180:183], v[116:119]
	v_mfma_f32_16x16x32_bf16 v[112:115], v[164:167], v[180:183], v[112:115]
	v_mfma_f32_16x16x32_bf16 v[100:103], v[146:149], v[188:191], v[100:103]
	v_mfma_f32_16x16x32_bf16 v[96:99], v[164:167], v[188:191], v[96:99]
	v_mfma_f32_16x16x32_bf16 v[84:87], v[146:149], v[196:199], v[84:87]
	v_mfma_f32_16x16x32_bf16 v[80:83], v[164:167], v[196:199], v[80:83]
	v_mfma_f32_16x16x32_bf16 v[132:135], v[160:163], v[176:179], v[132:135]
	v_mfma_f32_16x16x32_bf16 v[128:131], v[168:171], v[176:179], v[128:131]
	v_mfma_f32_16x16x32_bf16 v[116:119], v[160:163], v[184:187], v[116:119]
	v_mfma_f32_16x16x32_bf16 v[112:115], v[168:171], v[184:187], v[112:115]
	v_mfma_f32_16x16x32_bf16 v[100:103], v[160:163], v[192:195], v[100:103]
	v_mfma_f32_16x16x32_bf16 v[96:99], v[168:171], v[192:195], v[96:99]
	v_mfma_f32_16x16x32_bf16 v[84:87], v[160:163], v[200:203], v[84:87]
	v_mfma_f32_16x16x32_bf16 v[80:83], v[168:171], v[200:203], v[80:83]
	s_setprio 0
	s_barrier
	s_add_u32 s80, s74, 0x80
	s_addc_u32 s81, s75, 0
	v_mov_b32_e32 v150, v152
	s_add_i32 s69, s69, s23
	ds_read_b128 v[172:175], v157 offset:49152
	ds_read_b128 v[176:179], v157 offset:50176
	ds_read_b128 v[180:183], v157 offset:51200
	ds_read_b128 v[184:187], v157 offset:52224
	ds_read_b128 v[188:191], v157 offset:53248
	ds_read_b128 v[192:195], v157 offset:54272
	ds_read_b128 v[196:199], v157 offset:55296
	ds_read_b128 v[200:203], v157 offset:56320
	s_mov_b32 m0, s69
	s_nop 0
	global_load_lds_dwordx4 v150, s[80:81]
	s_add_u32 s80, s74, 0x20080
	s_addc_u32 s81, s75, 0
	s_add_i32 m0, s69, 0x2000
	s_nop 0
	global_load_lds_dwordx4 v152, s[80:81]
	s_add_u32 s80, s74, 0x40080
	s_addc_u32 s81, s75, 0
	s_add_i32 s69, s82, s23
	s_mov_b32 m0, s69
	s_add_u32 s74, s74, 0x60080
	global_load_lds_dwordx4 v152, s[80:81]
	s_addc_u32 s75, s75, 0
	s_add_i32 m0, s69, 0x2000
	s_add_u32 s70, s70, 0x20080
	global_load_lds_dwordx4 v152, s[74:75]
	s_mov_b32 m0, s43
	s_addc_u32 s71, s71, 0
	global_load_lds_dwordx4 v153, s[72:73]
	s_mov_b32 m0, s45
	s_nop 0
	global_load_lds_dwordx4 v153, s[70:71]
	s_waitcnt vmcnt(8)
	s_waitcnt lgkmcnt(0)
	s_barrier
	s_setprio 3
	v_mfma_f32_16x16x32_bf16 v[72:75], v[56:59], v[172:175], v[72:75]
	v_mfma_f32_16x16x32_bf16 v[64:67], v[68:71], v[172:175], v[64:67]
	v_mfma_f32_16x16x32_bf16 v[44:47], v[56:59], v[180:183], v[44:47]
	v_mfma_f32_16x16x32_bf16 v[40:43], v[68:71], v[180:183], v[40:43]
	v_mfma_f32_16x16x32_bf16 v[28:31], v[56:59], v[188:191], v[28:31]
	v_mfma_f32_16x16x32_bf16 v[24:27], v[68:71], v[188:191], v[24:27]
	v_mfma_f32_16x16x32_bf16 v[12:15], v[56:59], v[196:199], v[12:15]
	v_mfma_f32_16x16x32_bf16 v[8:11], v[68:71], v[196:199], v[8:11]
	v_mfma_f32_16x16x32_bf16 v[72:75], v[60:63], v[176:179], v[72:75]
	v_mfma_f32_16x16x32_bf16 v[64:67], v[76:79], v[176:179], v[64:67]
	v_mfma_f32_16x16x32_bf16 v[44:47], v[60:63], v[184:187], v[44:47]
	v_mfma_f32_16x16x32_bf16 v[40:43], v[76:79], v[184:187], v[40:43]
	v_mfma_f32_16x16x32_bf16 v[28:31], v[60:63], v[192:195], v[28:31]
	v_mfma_f32_16x16x32_bf16 v[24:27], v[76:79], v[192:195], v[24:27]
	v_mfma_f32_16x16x32_bf16 v[12:15], v[60:63], v[200:203], v[12:15]
	v_mfma_f32_16x16x32_bf16 v[8:11], v[76:79], v[200:203], v[8:11]
	v_mfma_f32_16x16x32_bf16 v[52:55], v[146:149], v[172:175], v[52:55]
	v_mfma_f32_16x16x32_bf16 v[48:51], v[164:167], v[172:175], v[48:51]
	v_mfma_f32_16x16x32_bf16 v[36:39], v[146:149], v[180:183], v[36:39]
	v_mfma_f32_16x16x32_bf16 v[32:35], v[164:167], v[180:183], v[32:35]
	v_mfma_f32_16x16x32_bf16 v[20:23], v[146:149], v[188:191], v[20:23]
	v_mfma_f32_16x16x32_bf16 v[16:19], v[164:167], v[188:191], v[16:19]
	v_mfma_f32_16x16x32_bf16 v[4:7], v[146:149], v[196:199], v[4:7]
	v_mfma_f32_16x16x32_bf16 v[0:3], v[164:167], v[196:199], v[0:3]
	v_mfma_f32_16x16x32_bf16 v[52:55], v[160:163], v[176:179], v[52:55]
	s_add_i32 s53, s53, 2
	v_mfma_f32_16x16x32_bf16 v[48:51], v[168:171], v[176:179], v[48:51]
	s_add_u32 s5, s5, 0x100
	v_mfma_f32_16x16x32_bf16 v[36:39], v[160:163], v[184:187], v[36:39]
	s_addc_u32 s51, s51, 0
	v_mfma_f32_16x16x32_bf16 v[32:35], v[168:171], v[184:187], v[32:35]
	s_add_u32 s6, s6, 0x100
	v_mfma_f32_16x16x32_bf16 v[20:23], v[160:163], v[192:195], v[20:23]
	s_addc_u32 s7, s7, 0
	v_mfma_f32_16x16x32_bf16 v[16:19], v[168:171], v[192:195], v[16:19]
	s_cmp_gt_u32 s53, 13
	v_mfma_f32_16x16x32_bf16 v[4:7], v[160:163], v[200:203], v[4:7]
	v_mfma_f32_16x16x32_bf16 v[0:3], v[168:171], v[200:203], v[0:3]
	s_setprio 0
	s_barrier
	s_cbranch_scc0 .LBB0_1769
	s_mov_b64 s[46:47], s[94:95]
	s_and_b64 vcc, exec, s[18:19]
	s_cbranch_vccz .LBB0_1772
	s_barrier

.LBB0_2137:
	ds_read_b128 v[8:11], v177
	ds_read_b128 v[12:15], v177 offset:1024
	ds_read_b128 v[136:139], v177 offset:2048
	ds_read_b128 v[140:143], v177 offset:3072
	ds_read_b128 v[146:149], v178
	ds_read_b128 v[150:153], v178 offset:1024
	ds_read_b128 v[154:157], v178 offset:2048
	ds_read_b128 v[158:161], v178 offset:3072
	s_add_u32 s30, s28, 0xfffa0080
	s_addc_u32 s31, s29, -1
	s_cmp_eq_u32 s65, 12
	s_cselect_b32 s30, s22, s30
	s_cselect_b32 s31, s23, s31
	s_cselect_b32 s36, s24, s19
	s_cselect_b32 s37, s25, s21
	s_add_u32 s34, s30, 0x80
	s_addc_u32 s35, s31, 0
	s_add_u32 s68, s28, 0xfffe0000
	v_mov_b32_e32 v170, v175
	s_addc_u32 s69, s29, -1
	ds_read_b128 v[162:165], v179
	ds_read_b128 v[166:169], v179 offset:1024
	ds_read_b128 v[180:183], v179 offset:2048
	ds_read_b128 v[184:187], v179 offset:3072
	ds_read_b128 v[188:191], v179 offset:4096
	ds_read_b128 v[192:195], v179 offset:5120
	ds_read_b128 v[196:199], v179 offset:6144
	ds_read_b128 v[200:203], v179 offset:7168
	s_add_i32 m0, s27, 0xc000
	s_nop 0
	global_load_lds_dwordx4 v170, s[68:69]
	s_mov_b64 s[68:69], s[28:29]
	s_add_i32 m0, s27, 0xe000
	s_nop 0
	global_load_lds_dwordx4 v175, s[68:69]
	s_waitcnt vmcnt(8)
	s_waitcnt lgkmcnt(0)
	s_barrier
	s_setprio 3
	v_mfma_f32_16x16x128_f8f6f4 v[132:135], v[8:15], v[162:169], v[132:135]
	v_mfma_f32_16x16x128_f8f6f4 v[128:131], v[136:143], v[162:169], v[128:131]
	v_mfma_f32_16x16x128_f8f6f4 v[116:119], v[8:15], v[180:187], v[116:119]
	v_mfma_f32_16x16x128_f8f6f4 v[112:115], v[136:143], v[180:187], v[112:115]
	v_mfma_f32_16x16x128_f8f6f4 v[100:103], v[8:15], v[188:195], v[100:103]
	v_mfma_f32_16x16x128_f8f6f4 v[96:99], v[136:143], v[188:195], v[96:99]
	v_mfma_f32_16x16x128_f8f6f4 v[84:87], v[8:15], v[196:203], v[84:87]
	v_mfma_f32_16x16x128_f8f6f4 v[80:83], v[136:143], v[196:203], v[80:83]
	v_mfma_f32_16x16x128_f8f6f4 v[124:127], v[146:153], v[162:169], v[124:127]
	v_mfma_f32_16x16x128_f8f6f4 v[120:123], v[154:161], v[162:169], v[120:123]
	v_mfma_f32_16x16x128_f8f6f4 v[108:111], v[146:153], v[180:187], v[108:111]
	v_mfma_f32_16x16x128_f8f6f4 v[104:107], v[154:161], v[180:187], v[104:107]
	v_mfma_f32_16x16x128_f8f6f4 v[92:95], v[146:153], v[188:195], v[92:95]
	v_mfma_f32_16x16x128_f8f6f4 v[88:91], v[154:161], v[188:195], v[88:91]
	v_mfma_f32_16x16x128_f8f6f4 v[76:79], v[146:153], v[196:203], v[76:79]
	v_mfma_f32_16x16x128_f8f6f4 v[72:75], v[154:161], v[196:203], v[72:75]
	s_setprio 0
	s_barrier
	v_mov_b32_e32 v170, v174
	s_mov_b64 s[68:69], s[36:37]
	s_add_i32 s70, s60, s39
	ds_read_b128 v[162:165], v179 offset:16384
	ds_read_b128 v[166:169], v179 offset:17408
	ds_read_b128 v[180:183], v179 offset:18432
	ds_read_b128 v[184:187], v179 offset:19456
	ds_read_b128 v[188:191], v179 offset:20480
	ds_read_b128 v[192:195], v179 offset:21504
	ds_read_b128 v[196:199], v179 offset:22528
	ds_read_b128 v[200:203], v179 offset:23552
	s_mov_b32 m0, s70
	s_nop 0
	global_load_lds_dwordx4 v170, s[68:69]
	s_add_u32 s68, s36, 0x20000
	s_addc_u32 s69, s37, 0
	s_add_i32 m0, s70, 0x2000
	s_nop 0
	global_load_lds_dwordx4 v174, s[68:69]
	s_add_u32 s68, s36, 0x40000
	s_addc_u32 s69, s37, 0
	s_add_i32 s70, s61, s39
	s_mov_b32 m0, s70
	s_nop 0
	global_load_lds_dwordx4 v174, s[68:69]
	s_add_u32 s68, s36, 0x60000
	s_addc_u32 s69, s37, 0
	s_add_i32 m0, s70, 0x2000
	s_nop 0
	global_load_lds_dwordx4 v174, s[68:69]
	s_mov_b64 s[68:69], s[30:31]
	s_mov_b32 m0, s27
	s_nop 0
	global_load_lds_dwordx4 v175, s[68:69]
	s_add_u32 s68, s30, 0x20000
	s_addc_u32 s69, s31, 0
	s_mov_b32 m0, s41
	s_nop 0
	global_load_lds_dwordx4 v175, s[68:69]
	s_waitcnt vmcnt(8)
	s_waitcnt lgkmcnt(0)
	s_barrier
	s_setprio 3
	v_mfma_f32_16x16x128_f8f6f4 v[68:71], v[8:15], v[162:169], v[68:71]
	v_mfma_f32_16x16x128_f8f6f4 v[64:67], v[136:143], v[162:169], v[64:67]
	v_mfma_f32_16x16x128_f8f6f4 v[52:55], v[8:15], v[180:187], v[52:55]
	v_mfma_f32_16x16x128_f8f6f4 v[48:51], v[136:143], v[180:187], v[48:51]
	v_mfma_f32_16x16x128_f8f6f4 v[36:39], v[8:15], v[188:195], v[36:39]
	v_mfma_f32_16x16x128_f8f6f4 v[32:35], v[136:143], v[188:195], v[32:35]
	v_mfma_f32_16x16x128_f8f6f4 v[20:23], v[8:15], v[196:203], v[20:23]
	v_mfma_f32_16x16x128_f8f6f4 v[16:19], v[136:143], v[196:203], v[16:19]
	v_mfma_f32_16x16x128_f8f6f4 v[60:63], v[146:153], v[162:169], v[60:63]
	v_mfma_f32_16x16x128_f8f6f4 v[56:59], v[154:161], v[162:169], v[56:59]
	v_mfma_f32_16x16x128_f8f6f4 v[44:47], v[146:153], v[180:187], v[44:47]
	v_mfma_f32_16x16x128_f8f6f4 v[40:43], v[154:161], v[180:187], v[40:43]
	v_mfma_f32_16x16x128_f8f6f4 v[28:31], v[146:153], v[188:195], v[28:31]
	v_mfma_f32_16x16x128_f8f6f4 v[24:27], v[154:161], v[188:195], v[24:27]
	v_mfma_f32_16x16x128_f8f6f4 v[136:139], v[146:153], v[196:203], v[4:7]
	v_mfma_f32_16x16x128_f8f6f4 v[140:143], v[154:161], v[196:203], v[0:3]
	s_setprio 0
	s_barrier
	s_add_i32 s70, 0, 0x18000
	s_add_i32 s71, 0, 0x1c000
	s_nop 2
	v_add_u32_e32 v0, s70, v176
	v_add_u32_e32 v12, s71, v176
	ds_read_b128 v[146:149], v0
	ds_read_b128 v[150:153], v0 offset:1024
	ds_read_b128 v[154:157], v0 offset:2048
	ds_read_b128 v[158:161], v0 offset:3072
	ds_read_b128 v[0:3], v12
	ds_read_b128 v[4:7], v12 offset:1024
	ds_read_b128 v[8:11], v12 offset:2048
	ds_read_b128 v[12:15], v12 offset:3072
	s_add_u32 s68, s30, 0x40000
	v_mov_b32_e32 v170, v175
	s_addc_u32 s69, s31, 0
	s_mov_b32 m0, s42
	ds_read_b128 v[162:165], v179 offset:32768
	ds_read_b128 v[166:169], v179 offset:33792
	ds_read_b128 v[180:183], v179 offset:34816
	ds_read_b128 v[184:187], v179 offset:35840
	ds_read_b128 v[188:191], v179 offset:36864
	ds_read_b128 v[192:195], v179 offset:37888
	ds_read_b128 v[196:199], v179 offset:38912
	ds_read_b128 v[200:203], v179 offset:39936
	s_nop 0
	global_load_lds_dwordx4 v170, s[68:69]
	s_add_u32 s68, s30, 0x60000
	s_addc_u32 s69, s31, 0
	s_mov_b32 m0, s43
	s_nop 0
	global_load_lds_dwordx4 v175, s[68:69]
	s_waitcnt vmcnt(8)
	s_waitcnt lgkmcnt(0)
	s_barrier
	s_setprio 3
	v_mfma_f32_16x16x128_f8f6f4 v[132:135], v[146:153], v[162:169], v[132:135]
	v_mfma_f32_16x16x128_f8f6f4 v[128:131], v[154:161], v[162:169], v[128:131]
	v_mfma_f32_16x16x128_f8f6f4 v[116:119], v[146:153], v[180:187], v[116:119]
	v_mfma_f32_16x16x128_f8f6f4 v[112:115], v[154:161], v[180:187], v[112:115]
	v_mfma_f32_16x16x128_f8f6f4 v[100:103], v[146:153], v[188:195], v[100:103]
	v_mfma_f32_16x16x128_f8f6f4 v[96:99], v[154:161], v[188:195], v[96:99]
	v_mfma_f32_16x16x128_f8f6f4 v[84:87], v[146:153], v[196:203], v[84:87]
	v_mfma_f32_16x16x128_f8f6f4 v[80:83], v[154:161], v[196:203], v[80:83]
	v_mfma_f32_16x16x128_f8f6f4 v[124:127], v[0:7], v[162:169], v[124:127]
	v_mfma_f32_16x16x128_f8f6f4 v[120:123], v[8:15], v[162:169], v[120:123]
	v_mfma_f32_16x16x128_f8f6f4 v[108:111], v[0:7], v[180:187], v[108:111]
	v_mfma_f32_16x16x128_f8f6f4 v[104:107], v[8:15], v[180:187], v[104:107]
	v_mfma_f32_16x16x128_f8f6f4 v[92:95], v[0:7], v[188:195], v[92:95]
	v_mfma_f32_16x16x128_f8f6f4 v[88:91], v[8:15], v[188:195], v[88:91]
	v_mfma_f32_16x16x128_f8f6f4 v[76:79], v[0:7], v[196:203], v[76:79]
	v_mfma_f32_16x16x128_f8f6f4 v[72:75], v[8:15], v[196:203], v[72:75]
	s_setprio 0
	s_barrier
	s_add_u32 s68, s36, 0x80
	s_addc_u32 s69, s37, 0
	v_mov_b32_e32 v170, v174
	s_add_i32 s70, s70, s39
	ds_read_b128 v[162:165], v179 offset:49152
	ds_read_b128 v[166:169], v179 offset:50176
	ds_read_b128 v[180:183], v179 offset:51200
	ds_read_b128 v[184:187], v179 offset:52224
	ds_read_b128 v[188:191], v179 offset:53248
	ds_read_b128 v[192:195], v179 offset:54272
	ds_read_b128 v[196:199], v179 offset:55296
	ds_read_b128 v[200:203], v179 offset:56320
	s_mov_b32 m0, s70
	s_nop 0
	global_load_lds_dwordx4 v170, s[68:69]
	s_add_u32 s68, s36, 0x20080
	s_addc_u32 s69, s37, 0
	s_add_i32 m0, s70, 0x2000
	s_nop 0
	global_load_lds_dwordx4 v174, s[68:69]
	s_add_u32 s68, s36, 0x40080
	s_addc_u32 s69, s37, 0
	s_add_i32 s70, s71, s39
	s_mov_b32 m0, s70
	s_add_u32 s36, s36, 0x60080
	global_load_lds_dwordx4 v174, s[68:69]
	s_addc_u32 s37, s37, 0
	s_add_i32 m0, s70, 0x2000
	s_add_u32 s30, s30, 0x20080
	global_load_lds_dwordx4 v174, s[36:37]
	s_mov_b32 m0, s53
	s_addc_u32 s31, s31, 0
	global_load_lds_dwordx4 v175, s[34:35]
	s_mov_b32 m0, s54
	s_nop 0
	global_load_lds_dwordx4 v175, s[30:31]
	s_waitcnt vmcnt(8)
	s_waitcnt lgkmcnt(0)
	s_barrier
	s_setprio 3
	v_mfma_f32_16x16x128_f8f6f4 v[68:71], v[146:153], v[162:169], v[68:71]
	v_mfma_f32_16x16x128_f8f6f4 v[64:67], v[154:161], v[162:169], v[64:67]
	v_mfma_f32_16x16x128_f8f6f4 v[52:55], v[146:153], v[180:187], v[52:55]
	v_mfma_f32_16x16x128_f8f6f4 v[48:51], v[154:161], v[180:187], v[48:51]
	v_mfma_f32_16x16x128_f8f6f4 v[36:39], v[146:153], v[188:195], v[36:39]
	v_mfma_f32_16x16x128_f8f6f4 v[32:35], v[154:161], v[188:195], v[32:35]
	v_mfma_f32_16x16x128_f8f6f4 v[20:23], v[146:153], v[196:203], v[20:23]
	v_mfma_f32_16x16x128_f8f6f4 v[16:19], v[154:161], v[196:203], v[16:19]
	v_mfma_f32_16x16x128_f8f6f4 v[60:63], v[0:7], v[162:169], v[60:63]
	s_add_i32 s65, s65, 2
	v_mfma_f32_16x16x128_f8f6f4 v[56:59], v[8:15], v[162:169], v[56:59]
	s_add_u32 s19, s19, 0x100
	v_mfma_f32_16x16x128_f8f6f4 v[44:47], v[0:7], v[180:187], v[44:47]
	s_addc_u32 s21, s21, 0
	v_mfma_f32_16x16x128_f8f6f4 v[40:43], v[8:15], v[180:187], v[40:43]
	s_add_u32 s28, s28, 0x100
	v_mfma_f32_16x16x128_f8f6f4 v[28:31], v[0:7], v[188:195], v[28:31]
	s_addc_u32 s29, s29, 0
	v_mfma_f32_16x16x128_f8f6f4 v[24:27], v[8:15], v[188:195], v[24:27]
	s_cmp_gt_u32 s65, 13
	v_mfma_f32_16x16x128_f8f6f4 v[4:7], v[0:7], v[196:203], v[136:139]
	v_mfma_f32_16x16x128_f8f6f4 v[0:3], v[8:15], v[196:203], v[140:143]
	s_setprio 0
	s_barrier
	s_cbranch_scc0 .LBB0_2137
	s_and_b64 vcc, exec, s[12:13]
	s_cbranch_vccz .LBB0_2140
	s_barrier

.LBB0_2446:
	ds_read_b128 v[144:147], v137
	ds_read_b128 v[148:151], v137 offset:1024
	ds_read_b128 v[152:155], v137 offset:2048
	ds_read_b128 v[156:159], v137 offset:3072
	ds_read_b128 v[160:163], v138
	ds_read_b128 v[164:167], v138 offset:1024
	ds_read_b128 v[168:171], v138 offset:2048
	ds_read_b128 v[172:175], v138 offset:3072
	s_cmp_eq_u32 s60, 4
	s_cselect_b64 vcc, -1, 0
	s_and_b64 s[22:23], vcc, exec
	s_cselect_b32 s26, s8, s58
	s_cselect_b32 s27, s9, s59
	s_cselect_b32 s24, s20, s14
	s_cselect_b32 s25, s21, s57
	s_add_u32 s22, s26, 0x80
	s_addc_u32 s23, s27, 0
	s_add_u32 s62, s58, 0xffffff80
	s_addc_u32 s63, s59, -1
	v_mov_b32_e32 v132, v130
	s_mov_b32 m0, s50
	ds_read_b128 v[176:179], v139
	ds_read_b128 v[180:183], v139 offset:1024
	ds_read_b128 v[184:187], v139 offset:2048
	ds_read_b128 v[188:191], v139 offset:3072
	ds_read_b128 v[192:195], v139 offset:4096
	ds_read_b128 v[196:199], v139 offset:5120
	ds_read_b128 v[200:203], v139 offset:6144
	ds_read_b128 v[204:207], v139 offset:7168
	s_mov_b64 s[64:65], s[62:63]
	s_nop 0
	global_load_lds_dwordx4 v132, s[64:65]
	s_mov_b32 m0, s51
	s_nop 0
	global_load_lds_dwordx4 v131, s[62:63]
	s_waitcnt vmcnt(8)
	s_waitcnt lgkmcnt(0)
	s_barrier
	s_setprio 3
	v_mfma_f32_16x16x128_f8f6f4 v[124:127], v[144:151], v[176:183], v[124:127]
	v_mfma_f32_16x16x128_f8f6f4 v[116:119], v[152:159], v[176:183], v[116:119]
	v_mfma_f32_16x16x128_f8f6f4 v[108:111], v[144:151], v[184:191], v[108:111]
	v_mfma_f32_16x16x128_f8f6f4 v[100:103], v[152:159], v[184:191], v[100:103]
	v_mfma_f32_16x16x128_f8f6f4 v[92:95], v[144:151], v[192:199], v[92:95]
	v_mfma_f32_16x16x128_f8f6f4 v[84:87], v[152:159], v[192:199], v[84:87]
	v_mfma_f32_16x16x128_f8f6f4 v[76:79], v[144:151], v[200:207], v[76:79]
	v_mfma_f32_16x16x128_f8f6f4 v[68:71], v[152:159], v[200:207], v[68:71]
	v_mfma_f32_16x16x128_f8f6f4 v[120:123], v[160:167], v[176:183], v[120:123]
	v_mfma_f32_16x16x128_f8f6f4 v[112:115], v[168:175], v[176:183], v[112:115]
	v_mfma_f32_16x16x128_f8f6f4 v[104:107], v[160:167], v[184:191], v[104:107]
	v_mfma_f32_16x16x128_f8f6f4 v[96:99], v[168:175], v[184:191], v[96:99]
	v_mfma_f32_16x16x128_f8f6f4 v[88:91], v[160:167], v[192:199], v[88:91]
	v_mfma_f32_16x16x128_f8f6f4 v[80:83], v[168:175], v[192:199], v[80:83]
	v_mfma_f32_16x16x128_f8f6f4 v[72:75], v[160:167], v[200:207], v[72:75]
	v_mfma_f32_16x16x128_f8f6f4 v[64:67], v[168:175], v[200:207], v[64:67]
	s_setprio 0
	s_barrier
	v_mov_b32_e32 v132, v134
	s_mov_b64 s[62:63], s[24:25]
	s_mov_b32 m0, s52
	ds_read_b128 v[176:179], v139 offset:16384
	ds_read_b128 v[180:183], v139 offset:17408
	ds_read_b128 v[184:187], v139 offset:18432
	ds_read_b128 v[188:191], v139 offset:19456
	ds_read_b128 v[192:195], v139 offset:20480
	ds_read_b128 v[196:199], v139 offset:21504
	ds_read_b128 v[200:203], v139 offset:22528
	ds_read_b128 v[204:207], v139 offset:23552
	s_nop 0
	global_load_lds_dwordx4 v132, s[62:63]
	s_add_u32 s62, s24, 0x10000
	s_addc_u32 s63, s25, 0
	s_add_i32 m0, s52, 0x2000
	s_nop 0
	global_load_lds_dwordx4 v134, s[62:63]
	s_add_u32 s62, s24, 0x20000
	s_addc_u32 s63, s25, 0
	s_add_i32 s61, s45, s34
	s_mov_b32 m0, s61
	s_nop 0
	global_load_lds_dwordx4 v134, s[62:63]
	s_add_u32 s62, s24, 0x30000
	s_addc_u32 s63, s25, 0
	s_add_i32 m0, s61, 0x2000
	s_nop 0
	global_load_lds_dwordx4 v134, s[62:63]
	v_cndmask_b32_e32 v132, v128, v141, vcc
	v_lshlrev_b32_e32 v133, 10, v132
	v_and_or_b32 v133, v133, s36, v135
	s_mov_b64 s[62:63], s[26:27]
	s_mov_b32 m0, s35
	s_nop 0
	global_load_lds_dwordx4 v133, s[62:63]
	v_cndmask_b32_e32 v143, v129, v142, vcc
	v_lshlrev_b32_e32 v208, 10, v143
	v_and_or_b32 v208, v208, s36, v135
	s_mov_b64 s[62:63], s[26:27]
	s_mov_b32 m0, s37
	s_nop 0
	global_load_lds_dwordx4 v208, s[62:63]
	s_waitcnt vmcnt(8)
	s_waitcnt lgkmcnt(0)
	s_barrier
	s_setprio 3
	v_mfma_f32_16x16x128_f8f6f4 v[60:63], v[144:151], v[176:183], v[60:63]
	v_mfma_f32_16x16x128_f8f6f4 v[52:55], v[152:159], v[176:183], v[52:55]
	v_mfma_f32_16x16x128_f8f6f4 v[44:47], v[144:151], v[184:191], v[44:47]
	v_mfma_f32_16x16x128_f8f6f4 v[36:39], v[152:159], v[184:191], v[36:39]
	v_mfma_f32_16x16x128_f8f6f4 v[28:31], v[144:151], v[192:199], v[28:31]
	v_mfma_f32_16x16x128_f8f6f4 v[20:23], v[152:159], v[192:199], v[20:23]
	v_mfma_f32_16x16x128_f8f6f4 v[12:15], v[144:151], v[200:207], v[12:15]
	v_mfma_f32_16x16x128_f8f6f4 v[4:7], v[152:159], v[200:207], v[4:7]
	v_mfma_f32_16x16x128_f8f6f4 v[56:59], v[160:167], v[176:183], v[56:59]
	v_mfma_f32_16x16x128_f8f6f4 v[48:51], v[168:175], v[176:183], v[48:51]
	v_mfma_f32_16x16x128_f8f6f4 v[40:43], v[160:167], v[184:191], v[40:43]
	v_mfma_f32_16x16x128_f8f6f4 v[32:35], v[168:175], v[184:191], v[32:35]
	v_mfma_f32_16x16x128_f8f6f4 v[24:27], v[160:167], v[192:199], v[24:27]
	v_mfma_f32_16x16x128_f8f6f4 v[16:19], v[168:175], v[192:199], v[16:19]
	v_mfma_f32_16x16x128_f8f6f4 v[8:11], v[160:167], v[200:207], v[8:11]
	v_mfma_f32_16x16x128_f8f6f4 v[0:3], v[168:175], v[200:207], v[0:3]
	s_setprio 0
	s_barrier
	s_add_i32 s61, 0, 0x18000
	s_add_i32 s64, 0, 0x1c000
	v_add_u32_e32 v156, s61, v136
	v_add_u32_e32 v172, s64, v136
	ds_read_b128 v[144:147], v156
	ds_read_b128 v[148:151], v156 offset:1024
	ds_read_b128 v[152:155], v156 offset:2048
	ds_read_b128 v[156:159], v156 offset:3072
	ds_read_b128 v[160:163], v172
	ds_read_b128 v[164:167], v172 offset:1024
	ds_read_b128 v[168:171], v172 offset:2048
	ds_read_b128 v[172:175], v172 offset:3072
	v_bfe_u32 v132, v132, 16, 16
	v_lshl_or_b32 v132, v132, 10, v135
	s_mov_b32 m0, s38
	ds_read_b128 v[176:179], v139 offset:32768
	ds_read_b128 v[180:183], v139 offset:33792
	ds_read_b128 v[184:187], v139 offset:34816
	ds_read_b128 v[188:191], v139 offset:35840
	ds_read_b128 v[192:195], v139 offset:36864
	ds_read_b128 v[196:199], v139 offset:37888
	ds_read_b128 v[200:203], v139 offset:38912
	ds_read_b128 v[204:207], v139 offset:39936
	s_mov_b64 s[62:63], s[26:27]
	s_nop 0
	global_load_lds_dwordx4 v132, s[62:63]
	v_bfe_u32 v132, v143, 16, 16
	v_lshl_or_b32 v132, v132, 10, v135
	s_mov_b32 m0, s39
	s_nop 0
	global_load_lds_dwordx4 v132, s[26:27]
	s_waitcnt vmcnt(8)
	s_waitcnt lgkmcnt(0)
	s_barrier
	s_setprio 3
	v_mfma_f32_16x16x128_f8f6f4 v[124:127], v[144:151], v[176:183], v[124:127]
	v_mfma_f32_16x16x128_f8f6f4 v[116:119], v[152:159], v[176:183], v[116:119]
	v_mfma_f32_16x16x128_f8f6f4 v[108:111], v[144:151], v[184:191], v[108:111]
	v_mfma_f32_16x16x128_f8f6f4 v[100:103], v[152:159], v[184:191], v[100:103]
	v_mfma_f32_16x16x128_f8f6f4 v[92:95], v[144:151], v[192:199], v[92:95]
	v_mfma_f32_16x16x128_f8f6f4 v[84:87], v[152:159], v[192:199], v[84:87]
	v_mfma_f32_16x16x128_f8f6f4 v[76:79], v[144:151], v[200:207], v[76:79]
	v_mfma_f32_16x16x128_f8f6f4 v[68:71], v[152:159], v[200:207], v[68:71]
	v_mfma_f32_16x16x128_f8f6f4 v[120:123], v[160:167], v[176:183], v[120:123]
	v_mfma_f32_16x16x128_f8f6f4 v[112:115], v[168:175], v[176:183], v[112:115]
	v_mfma_f32_16x16x128_f8f6f4 v[104:107], v[160:167], v[184:191], v[104:107]
	v_mfma_f32_16x16x128_f8f6f4 v[96:99], v[168:175], v[184:191], v[96:99]
	v_mfma_f32_16x16x128_f8f6f4 v[88:91], v[160:167], v[192:199], v[88:91]
	v_mfma_f32_16x16x128_f8f6f4 v[80:83], v[168:175], v[192:199], v[80:83]
	v_mfma_f32_16x16x128_f8f6f4 v[72:75], v[160:167], v[200:207], v[72:75]
	v_mfma_f32_16x16x128_f8f6f4 v[64:67], v[168:175], v[200:207], v[64:67]
	s_setprio 0
	s_barrier
	s_add_u32 s26, s24, 0x80
	s_addc_u32 s27, s25, 0
	v_mov_b32_e32 v132, v134
	s_add_i32 s61, s61, s34
	ds_read_b128 v[176:179], v139 offset:49152
	ds_read_b128 v[180:183], v139 offset:50176
	ds_read_b128 v[184:187], v139 offset:51200
	ds_read_b128 v[188:191], v139 offset:52224
	ds_read_b128 v[192:195], v139 offset:53248
	ds_read_b128 v[196:199], v139 offset:54272
	ds_read_b128 v[200:203], v139 offset:55296
	ds_read_b128 v[204:207], v139 offset:56320
	s_mov_b32 m0, s61
	s_nop 0
	global_load_lds_dwordx4 v132, s[26:27]
	s_add_u32 s26, s24, 0x10080
	s_addc_u32 s27, s25, 0
	s_add_i32 m0, s61, 0x2000
	s_nop 0
	global_load_lds_dwordx4 v134, s[26:27]
	s_add_u32 s26, s24, 0x20080
	s_addc_u32 s27, s25, 0
	s_add_i32 s61, s64, s34
	s_mov_b32 m0, s61
	s_add_u32 s24, s24, 0x30080
	s_addc_u32 s25, s25, 0
	global_load_lds_dwordx4 v134, s[26:27]
	s_add_i32 m0, s61, 0x2000
	s_nop 0
	global_load_lds_dwordx4 v134, s[24:25]
	s_mov_b64 s[24:25], s[22:23]
	s_mov_b32 m0, s42
	s_nop 0
	global_load_lds_dwordx4 v133, s[24:25]
	s_mov_b32 m0, s43
	s_nop 0
	global_load_lds_dwordx4 v208, s[22:23]
	s_waitcnt vmcnt(8)
	s_waitcnt lgkmcnt(0)
	s_barrier
	s_setprio 3
	v_mfma_f32_16x16x128_f8f6f4 v[60:63], v[144:151], v[176:183], v[60:63]
	v_mfma_f32_16x16x128_f8f6f4 v[52:55], v[152:159], v[176:183], v[52:55]
	v_mfma_f32_16x16x128_f8f6f4 v[44:47], v[144:151], v[184:191], v[44:47]
	v_mfma_f32_16x16x128_f8f6f4 v[36:39], v[152:159], v[184:191], v[36:39]
	v_mfma_f32_16x16x128_f8f6f4 v[28:31], v[144:151], v[192:199], v[28:31]
	v_mfma_f32_16x16x128_f8f6f4 v[20:23], v[152:159], v[192:199], v[20:23]
	v_mfma_f32_16x16x128_f8f6f4 v[12:15], v[144:151], v[200:207], v[12:15]
	v_mfma_f32_16x16x128_f8f6f4 v[4:7], v[152:159], v[200:207], v[4:7]
	v_mfma_f32_16x16x128_f8f6f4 v[56:59], v[160:167], v[176:183], v[56:59]
	s_add_i32 s60, s60, 2
	v_mfma_f32_16x16x128_f8f6f4 v[48:51], v[168:175], v[176:183], v[48:51]
	s_add_u32 s14, s14, 0x100
	v_mfma_f32_16x16x128_f8f6f4 v[40:43], v[160:167], v[184:191], v[40:43]
	s_addc_u32 s57, s57, 0
	v_mfma_f32_16x16x128_f8f6f4 v[32:35], v[168:175], v[184:191], v[32:35]
	s_add_u32 s58, s58, 0x100
	v_mfma_f32_16x16x128_f8f6f4 v[24:27], v[160:167], v[192:199], v[24:27]
	s_addc_u32 s59, s59, 0
	v_mfma_f32_16x16x128_f8f6f4 v[16:19], v[168:175], v[192:199], v[16:19]
	s_cmp_gt_u32 s60, 5
	v_mfma_f32_16x16x128_f8f6f4 v[8:11], v[160:167], v[200:207], v[8:11]
	v_mfma_f32_16x16x128_f8f6f4 v[0:3], v[168:175], v[200:207], v[0:3]
	s_setprio 0
	s_barrier
	s_cbranch_scc0 .LBB0_2446
	s_and_b64 vcc, exec, s[18:19]
	s_cbranch_vccz .LBB0_2449
	s_barrier

.LBB0_2608:
	ds_read_b128 v[72:75], v67
	ds_read_b128 v[76:79], v67 offset:1024
	ds_read_b128 v[80:83], v67 offset:2048
	ds_read_b128 v[84:87], v67 offset:3072
	ds_read_b128 v[88:91], v68
	ds_read_b128 v[92:95], v68 offset:1024
	ds_read_b128 v[96:99], v68 offset:2048
	ds_read_b128 v[100:103], v68 offset:3072
	s_cmp_eq_u32 s36, 4
	s_cselect_b32 s16, s8, s34
	s_cselect_b32 s17, s9, s35
	s_cselect_b32 s14, s0, s30
	s_cselect_b32 s15, s1, s31
	s_add_u32 s4, s16, 0x80
	s_addc_u32 s5, s17, 0
	ds_read_b128 v[104:107], v69
	ds_read_b128 v[108:111], v69 offset:1024
	ds_read_b128 v[112:115], v69 offset:2048
	ds_read_b128 v[116:119], v69 offset:3072
	ds_read_b128 v[120:123], v69 offset:4096
	ds_read_b128 v[124:127], v69 offset:5120
	ds_read_b128 v[128:131], v69 offset:6144
	ds_read_b128 v[132:135], v69 offset:7168
	s_waitcnt vmcnt(6)
	s_waitcnt lgkmcnt(0)
	s_barrier
	s_setprio 3
	v_mfma_f32_16x16x128_f8f6f4 v[60:63], v[72:79], v[104:111], v[60:63]
	v_mfma_f32_16x16x128_f8f6f4 v[52:55], v[80:87], v[104:111], v[52:55]
	v_mfma_f32_16x16x128_f8f6f4 v[44:47], v[72:79], v[112:119], v[44:47]
	v_mfma_f32_16x16x128_f8f6f4 v[36:39], v[80:87], v[112:119], v[36:39]
	v_mfma_f32_16x16x128_f8f6f4 v[28:31], v[72:79], v[120:127], v[28:31]
	v_mfma_f32_16x16x128_f8f6f4 v[20:23], v[80:87], v[120:127], v[20:23]
	v_mfma_f32_16x16x128_f8f6f4 v[12:15], v[72:79], v[128:135], v[12:15]
	v_mfma_f32_16x16x128_f8f6f4 v[136:139], v[80:87], v[128:135], v[4:7]
	v_mfma_f32_16x16x128_f8f6f4 v[56:59], v[88:95], v[104:111], v[56:59]
	v_mfma_f32_16x16x128_f8f6f4 v[48:51], v[96:103], v[104:111], v[48:51]
	v_mfma_f32_16x16x128_f8f6f4 v[40:43], v[88:95], v[112:119], v[40:43]
	v_mfma_f32_16x16x128_f8f6f4 v[32:35], v[96:103], v[112:119], v[32:35]
	v_mfma_f32_16x16x128_f8f6f4 v[24:27], v[88:95], v[120:127], v[24:27]
	v_mfma_f32_16x16x128_f8f6f4 v[16:19], v[96:103], v[120:127], v[16:19]
	v_mfma_f32_16x16x128_f8f6f4 v[8:11], v[88:95], v[128:135], v[8:11]
	v_mfma_f32_16x16x128_f8f6f4 v[128:131], v[96:103], v[128:135], v[0:3]
	s_setprio 0
	s_barrier
	s_nop 4
	s_mov_b64 s[50:51], s[14:15]
	s_mov_b32 m0, s37
	s_nop 0
	global_load_lds_dwordx4 v64, s[50:51]
	s_add_u32 s50, s14, 0x10000
	s_addc_u32 s51, s15, 0
	s_mov_b32 m0, s38
	s_nop 0
	global_load_lds_dwordx4 v64, s[50:51]
	s_add_u32 s50, s14, 0x20000
	s_addc_u32 s51, s15, 0
	s_mov_b32 m0, s39
	s_nop 0
	global_load_lds_dwordx4 v64, s[50:51]
	s_add_u32 s50, s14, 0x30000
	s_addc_u32 s51, s15, 0
	s_mov_b32 m0, s40
	s_nop 0
	global_load_lds_dwordx4 v64, s[50:51]
	s_mov_b64 s[50:51], s[16:17]
	s_mov_b32 m0, s23
	s_nop 0
	global_load_lds_dwordx4 v65, s[50:51]
	s_mov_b32 m0, s25
	s_nop 0
	global_load_lds_dwordx4 v66, s[16:17]
	s_waitcnt vmcnt(6)
	s_waitcnt lgkmcnt(0)
	s_barrier
	s_barrier
	ds_read_b128 v[0:3], v70
	ds_read_b128 v[4:7], v70 offset:1024
	ds_read_b128 v[72:75], v70 offset:2048
	ds_read_b128 v[76:79], v70 offset:3072
	ds_read_b128 v[80:83], v71
	ds_read_b128 v[84:87], v71 offset:1024
	ds_read_b128 v[88:91], v71 offset:2048
	ds_read_b128 v[92:95], v71 offset:3072
	ds_read_b128 v[96:99], v69 offset:32768
	ds_read_b128 v[100:103], v69 offset:33792
	ds_read_b128 v[104:107], v69 offset:34816
	ds_read_b128 v[108:111], v69 offset:35840
	ds_read_b128 v[112:115], v69 offset:36864
	ds_read_b128 v[116:119], v69 offset:37888
	ds_read_b128 v[120:123], v69 offset:38912
	ds_read_b128 v[124:127], v69 offset:39936
	s_waitcnt vmcnt(6)
	s_waitcnt lgkmcnt(0)
	s_barrier
	s_setprio 3
	v_mfma_f32_16x16x128_f8f6f4 v[60:63], v[0:7], v[96:103], v[60:63]
	v_mfma_f32_16x16x128_f8f6f4 v[52:55], v[72:79], v[96:103], v[52:55]
	v_mfma_f32_16x16x128_f8f6f4 v[44:47], v[0:7], v[104:111], v[44:47]
	v_mfma_f32_16x16x128_f8f6f4 v[36:39], v[72:79], v[104:111], v[36:39]
	v_mfma_f32_16x16x128_f8f6f4 v[28:31], v[0:7], v[112:119], v[28:31]
	v_mfma_f32_16x16x128_f8f6f4 v[20:23], v[72:79], v[112:119], v[20:23]
	v_mfma_f32_16x16x128_f8f6f4 v[12:15], v[0:7], v[120:127], v[12:15]
	v_mfma_f32_16x16x128_f8f6f4 v[4:7], v[72:79], v[120:127], v[136:139]
	v_mfma_f32_16x16x128_f8f6f4 v[56:59], v[80:87], v[96:103], v[56:59]
	s_add_u32 s16, s14, 0x80
	s_addc_u32 s17, s15, 0
	v_mfma_f32_16x16x128_f8f6f4 v[48:51], v[88:95], v[96:103], v[48:51]
	v_mfma_f32_16x16x128_f8f6f4 v[40:43], v[80:87], v[104:111], v[40:43]
	v_mfma_f32_16x16x128_f8f6f4 v[32:35], v[88:95], v[104:111], v[32:35]
	v_mfma_f32_16x16x128_f8f6f4 v[24:27], v[80:87], v[112:119], v[24:27]
	v_mfma_f32_16x16x128_f8f6f4 v[16:19], v[88:95], v[112:119], v[16:19]
	v_mfma_f32_16x16x128_f8f6f4 v[8:11], v[80:87], v[120:127], v[8:11]
	v_mfma_f32_16x16x128_f8f6f4 v[0:3], v[88:95], v[120:127], v[128:131]
	s_setprio 0
	s_barrier
	s_mov_b32 m0, s41
	s_nop 0
	global_load_lds_dwordx4 v64, s[16:17]
	s_add_u32 s16, s14, 0x10080
	s_addc_u32 s17, s15, 0
	s_mov_b32 m0, s42
	s_nop 0
	global_load_lds_dwordx4 v64, s[16:17]
	s_add_u32 s16, s14, 0x20080
	s_addc_u32 s17, s15, 0
	s_mov_b32 m0, s43
	s_add_u32 s14, s14, 0x30080
	global_load_lds_dwordx4 v64, s[16:17]
	s_addc_u32 s15, s15, 0
	s_mov_b32 m0, s44
	s_nop 0
	global_load_lds_dwordx4 v64, s[14:15]
	s_mov_b64 s[14:15], s[4:5]
	s_mov_b32 m0, s26
	s_nop 0
	global_load_lds_dwordx4 v65, s[14:15]
	s_mov_b32 m0, s27
	s_nop 0
	global_load_lds_dwordx4 v66, s[4:5]
	s_add_i32 s36, s36, 2
	s_add_u32 s30, s30, 0x100
	s_addc_u32 s31, s31, 0
	s_add_u32 s34, s34, 0x100
	s_addc_u32 s35, s35, 0
	s_cmp_gt_u32 s36, 5
	s_waitcnt vmcnt(6)
	s_waitcnt lgkmcnt(0)
	s_barrier
	s_barrier
	s_cbranch_scc0 .LBB0_2608
	s_cmpk_lt_u32 s22, 0x100
	s_cbranch_scc0 .LBB0_2611
	s_barrier
